# c14
# speedup vs baseline: 1.0120x; 1.0038x over previous
.LBB2_6:
	s_mov_b32 s6, 0
	s_ashr_i32 s7, s6, 31
	v_add_u32_e32 v144, s6, v0
	v_ashrrev_i32_e32 v0, 7, v144
	v_and_b32_e32 v0, -2, v0
	v_bfe_u32 v147, v144, 5, 1
	v_lshl_add_u32 v148, s14, 2, v0
	v_bfe_u32 v146, v144, 4, 1
	v_or_b32_e32 v0, v148, v147
	v_lshlrev_b32_e32 v42, 5, v0
	v_lshlrev_b32_e32 v0, 2, v146
	s_lshl_b64 s[4:5], s[6:7], 2
	v_or_b32_e32 v0, v42, v0
	s_add_u32 s0, s8, s4
	v_ashrrev_i32_e32 v1, 31, v0
	s_addc_u32 s1, s9, s5
	v_lshlrev_b64 v[38:39], 2, v[0:1]
	v_lshl_add_u64 v[150:151], s[0:1], 0, v[38:39]
	global_load_dwordx4 v[34:37], v[150:151], off
	s_add_u32 s4, s10, s4
	s_addc_u32 s5, s11, s5
	v_lshl_add_u64 v[152:153], s[4:5], 0, v[38:39]
	v_ashrrev_i32_e32 v1, 31, v42
	global_load_dwordx4 v[38:41], v[152:153], off
	v_lshlrev_b64 v[42:43], 2, v[0:1]
	v_lshl_add_u64 v[154:155], s[0:1], 0, v[42:43]
	v_lshl_add_u64 v[156:157], s[4:5], 0, v[42:43]
	global_load_dwordx4 v[42:45], v[154:155], off offset:64
	global_load_dwordx4 v[164:167], v[156:157], off offset:64
	global_load_dwordx4 v[168:171], v[154:155], off offset:32
	global_load_dwordx4 v[172:175], v[156:157], off offset:32
	v_or_b32_e32 v0, 8, v0
	v_lshlrev_b64 v[0:1], 2, v[0:1]
	v_lshl_add_u64 v[158:159], s[0:1], 0, v[0:1]
	v_lshl_add_u64 v[160:161], s[4:5], 0, v[0:1]
	global_load_dwordx4 v[176:179], v[158:159], off offset:64
	global_load_dwordx4 v[180:183], v[160:161], off offset:64
	v_ashrrev_i32_e32 v0, 1, v148
	v_lshl_add_u32 v0, s2, 6, v0
	s_movk_i32 s3, 0x6000
	v_mov_b64_e32 v[46:47], s[12:13]
	v_ashrrev_i32_e32 v1, 31, v0
	v_mad_i64_i32 v[148:149], s[2:3], v0, s3, v[46:47]
	v_lshlrev_b64 v[0:1], 10, v[0:1]
	s_mov_b64 s[6:7], 0x3000000
	v_permlane32_swap_b32_e32 v30, v14
	v_permlane32_swap_b32_e32 v31, v15
	v_lshl_add_u64 v[0:1], s[12:13], 0, v[0:1]
	v_permlane32_swap_b32_e32 v32, v16
	v_permlane32_swap_b32_e32 v33, v17
	s_mov_b32 s4, 0xbfb8aa3b
	v_and_b32_e32 v163, 0xcf, v144
	v_lshlrev_b32_e32 v162, 9, v147
	v_mul_u32_u24_e32 v144, 12, v146
	v_cmp_eq_u32_e64 s[0:1], 0, v146
	v_lshl_add_u64 v[146:147], v[0:1], 0, s[6:7]
	v_permlane32_swap_b32_e32 v26, v10
	v_permlane32_swap_b32_e32 v27, v11
	v_permlane32_swap_b32_e32 v22, v6
	v_permlane32_swap_b32_e32 v23, v7
	v_permlane32_swap_b32_e32 v28, v12
	v_permlane32_swap_b32_e32 v29, v13
	v_permlane32_swap_b32_e32 v24, v8
	v_permlane32_swap_b32_e32 v25, v9
	v_permlane32_swap_b32_e32 v18, v2
	v_permlane32_swap_b32_e32 v19, v3
	v_permlane32_swap_b32_e32 v20, v4
	v_permlane32_swap_b32_e32 v21, v5
	s_mov_b32 s3, 0x700000
	s_mov_b32 s8, 0x42000000
	s_mov_b32 s2, 0xc2000000
	v_mov_b32_e32 v145, 0
	s_waitcnt vmcnt(0)
	v_pk_mul_f32 v[0:1], v[34:35], v[30:31]
	v_pk_mul_f32 v[30:31], v[36:37], v[32:33]
	v_pk_mul_f32 v[32:33], v[0:1], s[4:5] op_sel_hi:[1,0]
	v_pk_mul_f32 v[34:35], v[30:31], s[4:5] op_sel_hi:[1,0]
	v_exp_f32_e32 v32, v32
	v_exp_f32_e32 v33, v33
	v_exp_f32_e32 v34, v34
	v_exp_f32_e32 v35, v35
	v_pk_mul_f32 v[26:27], v[38:39], v[26:27]
	v_pk_add_f32 v[32:33], v[32:33], 1.0 op_sel_hi:[1,0]
	v_pk_mul_f32 v[22:23], v[42:43], v[22:23]
	v_rcp_f32_e32 v32, v32
	v_rcp_f32_e32 v33, v33
	v_pk_add_f32 v[34:35], v[34:35], 1.0 op_sel_hi:[1,0]
	v_pk_mul_f32 v[24:25], v[44:45], v[24:25]
	v_rcp_f32_e32 v34, v34
	v_rcp_f32_e32 v35, v35
	v_pk_mul_f32 v[0:1], v[0:1], v[32:33]
	v_pk_mul_f32 v[18:19], v[164:165], v[18:19]
	v_pk_mul_f32 v[0:1], v[26:27], v[0:1]
	v_pk_mul_f32 v[26:27], v[40:41], v[28:29]
	v_pk_mul_f32 v[28:29], v[30:31], v[34:35]
	v_pk_mul_f32 v[30:31], v[24:25], s[4:5] op_sel_hi:[1,0]
	v_pk_mul_f32 v[26:27], v[26:27], v[28:29]
	v_pk_mul_f32 v[28:29], v[22:23], s[4:5] op_sel_hi:[1,0]
	v_exp_f32_e32 v30, v30
	v_exp_f32_e32 v28, v28
	v_exp_f32_e32 v29, v29
	v_exp_f32_e32 v31, v31
	v_pk_mul_f32 v[20:21], v[166:167], v[20:21]
	v_pk_mul_f32 v[14:15], v[168:169], v[14:15]
	v_pk_add_f32 v[28:29], v[28:29], 1.0 op_sel_hi:[1,0]
	v_pk_add_f32 v[30:31], v[30:31], 1.0 op_sel_hi:[1,0]
	v_rcp_f32_e32 v28, v28
	v_rcp_f32_e32 v29, v29
	v_rcp_f32_e32 v30, v30
	v_rcp_f32_e32 v31, v31
	v_pk_mul_f32 v[16:17], v[170:171], v[16:17]
	v_pk_mul_f32 v[22:23], v[22:23], v[28:29]
	v_pk_mul_f32 v[10:11], v[172:173], v[10:11]
	v_pk_mul_f32 v[18:19], v[18:19], v[22:23]
	v_pk_mul_f32 v[22:23], v[24:25], v[30:31]
	v_pk_mul_f32 v[24:25], v[16:17], s[4:5] op_sel_hi:[1,0]
	v_pk_mul_f32 v[20:21], v[20:21], v[22:23]
	v_pk_mul_f32 v[22:23], v[14:15], s[4:5] op_sel_hi:[1,0]
	v_exp_f32_e32 v24, v24
	v_exp_f32_e32 v22, v22
	v_exp_f32_e32 v23, v23
	v_exp_f32_e32 v25, v25
	v_pk_mul_f32 v[12:13], v[174:175], v[12:13]
	v_pk_mul_f32 v[6:7], v[176:177], v[6:7]
	v_pk_add_f32 v[22:23], v[22:23], 1.0 op_sel_hi:[1,0]
	v_pk_add_f32 v[24:25], v[24:25], 1.0 op_sel_hi:[1,0]
	v_rcp_f32_e32 v22, v22
	v_rcp_f32_e32 v23, v23
	v_rcp_f32_e32 v24, v24
	v_rcp_f32_e32 v25, v25
	v_pk_mul_f32 v[8:9], v[178:179], v[8:9]
	v_pk_mul_f32 v[14:15], v[14:15], v[22:23]
	v_pk_mul_f32 v[2:3], v[180:181], v[2:3]
	v_pk_mul_f32 v[10:11], v[10:11], v[14:15]
	v_pk_mul_f32 v[14:15], v[16:17], v[24:25]
	v_pk_mul_f32 v[16:17], v[8:9], s[4:5] op_sel_hi:[1,0]
	v_pk_mul_f32 v[12:13], v[12:13], v[14:15]
	v_pk_mul_f32 v[14:15], v[6:7], s[4:5] op_sel_hi:[1,0]
	v_exp_f32_e32 v16, v16
	v_exp_f32_e32 v14, v14
	v_exp_f32_e32 v15, v15
	v_exp_f32_e32 v17, v17
	v_pk_mul_f32 v[4:5], v[182:183], v[4:5]
	v_mov_b32_e32 v164, 0xffffff7f
	v_pk_add_f32 v[14:15], v[14:15], 1.0 op_sel_hi:[1,0]
	v_pk_add_f32 v[16:17], v[16:17], 1.0 op_sel_hi:[1,0]
	v_rcp_f32_e32 v14, v14
	v_rcp_f32_e32 v15, v15
	v_rcp_f32_e32 v16, v16
	v_rcp_f32_e32 v17, v17
	s_movk_i32 s5, 0xff9c
	v_pk_mul_f32 v[6:7], v[6:7], v[14:15]
	v_mov_b32_e32 v165, 0x64
	v_pk_mul_f32 v[2:3], v[2:3], v[6:7]
	v_pk_mul_f32 v[6:7], v[8:9], v[16:17]
	v_pk_mul_f32 v[4:5], v[4:5], v[6:7]
	v_max3_f32 v6, |v20|, |v21|, |v0|
	v_max3_f32 v6, v6, |v1|, |v26|
	v_max3_f32 v6, v6, |v27|, |v18|
	v_max3_f32 v6, v6, |v19|, |v10|
	v_max3_f32 v6, v6, |v11|, |v12|
	v_max3_f32 v6, v6, |v13|, |v2|
	v_max3_f32 v6, v6, |v3|, |v4|
	v_max_f32_e64 v6, v6, |v5|
	v_mov_b32_e32 v7, v6
	s_nop 1
	v_permlane16_swap_b32_e32 v6, v7
	v_max_f32_e32 v6, v6, v7
	v_lshrrev_b32_e32 v7, 23, v6
	v_and_b32_e32 v6, 0x7fffff, v6
	v_cmp_lt_u32_e32 vcc, s3, v6
	s_nop 1
	v_addc_co_u32_e32 v6, vcc, v7, v164, vcc
	v_med3_i32 v166, v6, s5, v165
	v_lshlrev_b32_e32 v6, 23, v166
	v_sub_u32_e32 v6, 1.0, v6
	v_pk_mul_f32 v[40:41], v[6:7], v[10:11] op_sel_hi:[0,1]
	v_pk_mul_f32 v[42:43], v[6:7], v[12:13] op_sel_hi:[0,1]
	v_pk_mul_f32 v[44:45], v[6:7], v[2:3] op_sel_hi:[0,1]
	v_pk_mul_f32 v[46:47], v[6:7], v[4:5] op_sel_hi:[0,1]
	v_pk_mul_f32 v[32:33], v[6:7], v[0:1] op_sel_hi:[0,1]
	v_pk_mul_f32 v[34:35], v[6:7], v[26:27] op_sel_hi:[0,1]
	v_pk_mul_f32 v[36:37], v[6:7], v[18:19] op_sel_hi:[0,1]
	v_pk_mul_f32 v[38:39], v[6:7], v[20:21] op_sel_hi:[0,1]
	v_cvt_scalef32_2xpk16_fp6_f32 v[168:173], v[32:47], v[40:55], 1.0
	v_cvt_scalef32_pk32_f32_fp6 v[0:31], v[168:173], s8
	v_fma_f32 v16, v32, s2, v0
	v_fma_f32 v17, v33, s2, v2
	v_fma_f32 v18, v34, s2, v4
	v_fma_f32 v19, v35, s2, v6
	v_fma_f32 v20, v36, s2, v8
	v_fma_f32 v21, v37, s2, v10
	v_fma_f32 v22, v38, s2, v12
	v_fma_f32 v23, v39, s2, v14
	v_fma_f32 v24, v40, s2, v1
	v_fma_f32 v25, v41, s2, v3
	v_fma_f32 v26, v42, s2, v5
	v_fma_f32 v27, v43, s2, v7
	v_fma_f32 v28, v44, s2, v9
	v_fma_f32 v29, v45, s2, v11
	v_fma_f32 v30, v46, s2, v13
	v_fma_f32 v31, v47, s2, v15
	v_cvt_scalef32_2xpk16_fp6_f32 v[0:5], v[16:31], v[24:39], 1.0
	v_or_b32_e32 v3, v163, v162
	v_mul_u32_u24_e32 v4, 24, v3
	v_mov_b32_e32 v5, v145
	v_lshl_add_u64 v[4:5], v[148:149], 0, v[4:5]
	v_lshl_add_u64 v[4:5], v[4:5], 0, v[144:145]
	global_store_dwordx3 v[4:5], v[168:170], off nt
	v_add_co_u32_e32 v4, vcc, 0x1000, v4
	v_xor_b32_e32 v0, 0x20820820, v0
	v_xor_b32_e32 v1, 0x8208208, v1
	v_xor_b32_e32 v2, 0x82082082, v2
	v_addc_co_u32_e32 v5, vcc, 0, v5, vcc
	global_store_dwordx3 v[4:5], v[0:2], off offset:2048 nt
	s_and_saveexec_b64 s[6:7], s[0:1]
	s_cbranch_execz .LBB2_8
	v_mov_b32_e32 v1, 0x7a00
	v_add_u32_e32 v0, 0x7f, v166
	v_lshl_add_u32 v1, v166, 8, v1
	v_or_b32_e32 v2, v1, v0
	v_lshl_or_b32 v0, v163, 1, v162
	v_mov_b32_e32 v1, v145
	v_lshl_add_u64 v[0:1], v[146:147], 0, v[0:1]
	global_store_short v[0:1], v2, off
.LBB2_8:
	s_or_b64 exec, exec, s[6:7]
	global_load_dwordx4 v[0:3], v[150:151], off
	global_load_dwordx4 v[4:7], v[152:153], off
	global_load_dwordx4 v[8:11], v[154:155], off offset:64
	global_load_dwordx4 v[12:15], v[156:157], off offset:64
	global_load_dwordx4 v[16:19], v[154:155], off offset:32
	global_load_dwordx4 v[20:23], v[156:157], off offset:32
	global_load_dwordx4 v[24:27], v[158:159], off offset:64
	global_load_dwordx4 v[28:31], v[160:161], off offset:64
	v_permlane32_swap_b32_e32 v132, v124
	v_permlane32_swap_b32_e32 v133, v125
	v_permlane32_swap_b32_e32 v128, v116
	v_permlane32_swap_b32_e32 v129, v117
	v_permlane32_swap_b32_e32 v134, v126
	v_permlane32_swap_b32_e32 v135, v127
	v_permlane32_swap_b32_e32 v130, v118
	v_permlane32_swap_b32_e32 v131, v119
	v_permlane32_swap_b32_e32 v140, v120
	v_permlane32_swap_b32_e32 v141, v121
	v_permlane32_swap_b32_e32 v136, v112
	v_permlane32_swap_b32_e32 v137, v113
	v_permlane32_swap_b32_e32 v142, v122
	v_permlane32_swap_b32_e32 v143, v123
	v_permlane32_swap_b32_e32 v138, v114
	v_permlane32_swap_b32_e32 v139, v115
	s_waitcnt vmcnt(7)
	v_pk_mul_f32 v[0:1], v[0:1], v[132:133]
	s_nop 0
	v_pk_mul_f32 v[32:33], v[0:1], s[4:5] op_sel_hi:[1,0]
	s_waitcnt vmcnt(5)
	v_pk_mul_f32 v[8:9], v[8:9], v[128:129]
	v_exp_f32_e32 v32, v32
	v_pk_mul_f32 v[36:37], v[8:9], s[4:5] op_sel_hi:[1,0]
	v_exp_f32_e32 v33, v33
	v_exp_f32_e32 v36, v36
	v_exp_f32_e32 v37, v37
	s_waitcnt vmcnt(3)
	v_pk_mul_f32 v[18:19], v[18:19], v[126:127]
	v_pk_mul_f32 v[2:3], v[2:3], v[134:135]
	v_pk_mul_f32 v[10:11], v[10:11], v[130:131]
	v_pk_mul_f32 v[42:43], v[18:19], s[4:5] op_sel_hi:[1,0]
	v_pk_add_f32 v[32:33], v[32:33], 1.0 op_sel_hi:[1,0]
	v_pk_add_f32 v[36:37], v[36:37], 1.0 op_sel_hi:[1,0]
	v_pk_mul_f32 v[16:17], v[16:17], v[124:125]
	v_pk_mul_f32 v[34:35], v[2:3], s[4:5] op_sel_hi:[1,0]
	v_pk_mul_f32 v[38:39], v[10:11], s[4:5] op_sel_hi:[1,0]
	v_exp_f32_e32 v42, v42
	v_exp_f32_e32 v43, v43
	v_rcp_f32_e32 v32, v32
	v_rcp_f32_e32 v33, v33
	v_rcp_f32_e32 v36, v36
	v_rcp_f32_e32 v37, v37
	v_pk_mul_f32 v[40:41], v[16:17], s[4:5] op_sel_hi:[1,0]
	v_exp_f32_e32 v34, v34
	v_exp_f32_e32 v35, v35
	v_exp_f32_e32 v38, v38
	v_exp_f32_e32 v39, v39
	v_exp_f32_e32 v40, v40
	v_exp_f32_e32 v41, v41
	v_pk_mul_f32 v[4:5], v[4:5], v[140:141]
	v_pk_mul_f32 v[12:13], v[12:13], v[136:137]
	v_pk_add_f32 v[42:43], v[42:43], 1.0 op_sel_hi:[1,0]
	v_pk_mul_f32 v[0:1], v[0:1], v[32:33]
	v_pk_mul_f32 v[8:9], v[8:9], v[36:37]
	v_pk_add_f32 v[34:35], v[34:35], 1.0 op_sel_hi:[1,0]
	v_pk_add_f32 v[38:39], v[38:39], 1.0 op_sel_hi:[1,0]
	v_pk_mul_f32 v[0:1], v[4:5], v[0:1]
	v_pk_mul_f32 v[4:5], v[12:13], v[8:9]
	v_rcp_f32_e32 v8, v42
	v_rcp_f32_e32 v9, v43
	v_pk_add_f32 v[40:41], v[40:41], 1.0 op_sel_hi:[1,0]
	v_rcp_f32_e32 v34, v34
	v_rcp_f32_e32 v35, v35
	v_rcp_f32_e32 v38, v38
	v_rcp_f32_e32 v39, v39
	v_rcp_f32_e32 v40, v40
	v_rcp_f32_e32 v41, v41
	s_waitcnt vmcnt(2)
	v_pk_mul_f32 v[12:13], v[22:23], v[122:123]
	v_pk_mul_f32 v[8:9], v[18:19], v[8:9]
	v_pk_mul_f32 v[6:7], v[6:7], v[142:143]
	v_pk_mul_f32 v[14:15], v[14:15], v[138:139]
	v_pk_mul_f32 v[2:3], v[2:3], v[34:35]
	v_pk_mul_f32 v[10:11], v[10:11], v[38:39]
	v_pk_mul_f32 v[8:9], v[12:13], v[8:9]
	s_waitcnt vmcnt(1)
	v_pk_mul_f32 v[12:13], v[24:25], v[116:117]
	v_pk_mul_f32 v[20:21], v[20:21], v[120:121]
	v_pk_mul_f32 v[2:3], v[6:7], v[2:3]
	v_pk_mul_f32 v[6:7], v[14:15], v[10:11]
	v_pk_mul_f32 v[10:11], v[16:17], v[40:41]
	v_pk_mul_f32 v[16:17], v[12:13], s[4:5] op_sel_hi:[1,0]
	v_pk_mul_f32 v[18:19], v[26:27], v[118:119]
	v_pk_mul_f32 v[10:11], v[20:21], v[10:11]
	v_exp_f32_e32 v16, v16
	v_exp_f32_e32 v17, v17
	v_pk_mul_f32 v[20:21], v[18:19], s[4:5] op_sel_hi:[1,0]
	s_waitcnt vmcnt(0)
	v_pk_mul_f32 v[14:15], v[28:29], v[112:113]
	v_exp_f32_e32 v20, v20
	v_exp_f32_e32 v21, v21
	v_pk_add_f32 v[16:17], v[16:17], 1.0 op_sel_hi:[1,0]
	v_pk_add_f32 v[20:21], v[20:21], 1.0 op_sel_hi:[1,0]
	v_rcp_f32_e32 v16, v16
	v_rcp_f32_e32 v17, v17
	v_rcp_f32_e32 v20, v20
	v_rcp_f32_e32 v21, v21
	v_pk_mul_f32 v[12:13], v[12:13], v[16:17]
	s_nop 0
	v_pk_mul_f32 v[12:13], v[14:15], v[12:13]
	v_pk_mul_f32 v[14:15], v[30:31], v[114:115]
	v_pk_mul_f32 v[16:17], v[18:19], v[20:21]
	v_pk_mul_f32 v[14:15], v[14:15], v[16:17]
	v_max3_f32 v16, |v6|, |v7|, |v0|
	v_max3_f32 v16, v16, |v1|, |v2|
	v_max3_f32 v16, v16, |v3|, |v4|
	v_max3_f32 v16, v16, |v5|, |v10|
	v_max3_f32 v16, v16, |v11|, |v8|
	v_max3_f32 v16, v16, |v9|, |v12|
	v_max3_f32 v16, v16, |v13|, |v14|
	v_max_f32_e64 v16, v16, |v15|
	v_mov_b32_e32 v17, v16
	s_nop 1
	v_permlane16_swap_b32_e32 v16, v17
	v_max_f32_e32 v16, v16, v17
	v_lshrrev_b32_e32 v17, 23, v16
	v_and_b32_e32 v16, 0x7fffff, v16
	v_cmp_lt_u32_e32 vcc, s3, v16
	s_nop 1
	v_addc_co_u32_e32 v16, vcc, v17, v164, vcc
	v_med3_i32 v112, v16, s5, v165
	v_lshlrev_b32_e32 v16, 23, v112
	v_sub_u32_e32 v16, 1.0, v16
	v_pk_mul_f32 v[40:41], v[16:17], v[10:11] op_sel_hi:[0,1]
	v_pk_mul_f32 v[42:43], v[16:17], v[8:9] op_sel_hi:[0,1]
	v_pk_mul_f32 v[44:45], v[16:17], v[12:13] op_sel_hi:[0,1]
	v_pk_mul_f32 v[46:47], v[16:17], v[14:15] op_sel_hi:[0,1]
	v_pk_mul_f32 v[32:33], v[16:17], v[0:1] op_sel_hi:[0,1]
	v_pk_mul_f32 v[34:35], v[16:17], v[2:3] op_sel_hi:[0,1]
	v_pk_mul_f32 v[36:37], v[16:17], v[4:5] op_sel_hi:[0,1]
	v_pk_mul_f32 v[38:39], v[16:17], v[6:7] op_sel_hi:[0,1]
	v_cvt_scalef32_2xpk16_fp6_f32 v[114:119], v[32:47], v[40:55], 1.0
	v_cvt_scalef32_pk32_f32_fp6 v[0:31], v[114:119], s8
	v_fma_f32 v16, v32, s2, v0
	v_fma_f32 v17, v33, s2, v2
	v_fma_f32 v18, v34, s2, v4
	v_fma_f32 v19, v35, s2, v6
	v_fma_f32 v20, v36, s2, v8
	v_fma_f32 v21, v37, s2, v10
	v_fma_f32 v22, v38, s2, v12
	v_fma_f32 v23, v39, s2, v14
	v_fma_f32 v24, v40, s2, v1
	v_fma_f32 v25, v41, s2, v3
	v_fma_f32 v26, v42, s2, v5
	v_fma_f32 v27, v43, s2, v7
	v_fma_f32 v28, v44, s2, v9
	v_fma_f32 v29, v45, s2, v11
	v_fma_f32 v30, v46, s2, v13
	v_fma_f32 v31, v47, s2, v15
	v_cvt_scalef32_2xpk16_fp6_f32 v[0:5], v[16:31], v[24:39], 1.0
	v_xor_b32_e32 v4, 0x20820820, v0
	v_or_b32_e32 v0, 16, v163
	v_xor_b32_e32 v5, 0x8208208, v1
	v_or_b32_e32 v1, v0, v162
	v_xor_b32_e32 v6, 0x82082082, v2
	v_mul_u32_u24_e32 v2, 24, v1
	v_mov_b32_e32 v3, v145
	v_lshl_add_u64 v[2:3], v[148:149], 0, v[2:3]
	v_lshl_add_u64 v[2:3], v[2:3], 0, v[144:145]
	global_store_dwordx3 v[2:3], v[114:116], off nt
	v_add_co_u32_e32 v2, vcc, 0x1000, v2
	s_nop 1
	v_addc_co_u32_e32 v3, vcc, 0, v3, vcc
	global_store_dwordx3 v[2:3], v[4:6], off offset:2048 nt
	s_and_saveexec_b64 s[2:3], s[0:1]
	s_cbranch_execz .LBB2_10
	v_mov_b32_e32 v2, 0x7a00
	v_add_u32_e32 v1, 0x7f, v112
	v_lshl_add_u32 v2, v112, 8, v2
	v_or_b32_e32 v2, v2, v1
	v_lshl_or_b32 v0, v0, 1, v162
	v_mov_b32_e32 v1, 0
	v_lshl_add_u64 v[0:1], v[146:147], 0, v[0:1]
	global_store_short v[0:1], v2, off
.LBB2_10:
	s_or_b64 exec, exec, s[2:3]
	global_load_dwordx4 v[0:3], v[150:151], off
	global_load_dwordx4 v[4:7], v[152:153], off
	global_load_dwordx4 v[8:11], v[154:155], off offset:64
	global_load_dwordx4 v[12:15], v[156:157], off offset:64
	global_load_dwordx4 v[16:19], v[154:155], off offset:32
	global_load_dwordx4 v[20:23], v[156:157], off offset:32
	global_load_dwordx4 v[24:27], v[158:159], off offset:64
	global_load_dwordx4 v[28:31], v[160:161], off offset:64
	v_permlane32_swap_b32_e32 v100, v92
	v_permlane32_swap_b32_e32 v101, v93
	v_permlane32_swap_b32_e32 v96, v84
	v_permlane32_swap_b32_e32 v97, v85
	s_mov_b32 s2, 0xbfb8aa3b
	v_permlane32_swap_b32_e32 v102, v94
	v_permlane32_swap_b32_e32 v103, v95
	v_permlane32_swap_b32_e32 v98, v86
	v_permlane32_swap_b32_e32 v99, v87
	v_permlane32_swap_b32_e32 v108, v88
	v_permlane32_swap_b32_e32 v109, v89
	v_permlane32_swap_b32_e32 v104, v80
	v_permlane32_swap_b32_e32 v105, v81
	v_permlane32_swap_b32_e32 v110, v90
	v_permlane32_swap_b32_e32 v111, v91
	v_permlane32_swap_b32_e32 v106, v82
	v_permlane32_swap_b32_e32 v107, v83
	s_mov_b32 s4, 0xc2000000
	s_waitcnt vmcnt(7)
	v_pk_mul_f32 v[0:1], v[0:1], v[100:101]
	s_nop 0
	v_pk_mul_f32 v[32:33], v[0:1], s[2:3] op_sel_hi:[1,0]
	s_waitcnt vmcnt(5)
	v_pk_mul_f32 v[8:9], v[8:9], v[96:97]
	v_exp_f32_e32 v32, v32
	v_pk_mul_f32 v[36:37], v[8:9], s[2:3] op_sel_hi:[1,0]
	v_exp_f32_e32 v33, v33
	v_exp_f32_e32 v36, v36
	v_exp_f32_e32 v37, v37
	s_waitcnt vmcnt(3)
	v_pk_mul_f32 v[18:19], v[18:19], v[94:95]
	v_pk_add_f32 v[32:33], v[32:33], 1.0 op_sel_hi:[1,0]
	v_pk_mul_f32 v[2:3], v[2:3], v[102:103]
	v_pk_add_f32 v[36:37], v[36:37], 1.0 op_sel_hi:[1,0]
	v_pk_mul_f32 v[10:11], v[10:11], v[98:99]
	v_pk_mul_f32 v[42:43], v[18:19], s[2:3] op_sel_hi:[1,0]
	v_rcp_f32_e32 v32, v32
	v_rcp_f32_e32 v33, v33
	v_rcp_f32_e32 v36, v36
	v_rcp_f32_e32 v37, v37
	v_pk_mul_f32 v[16:17], v[16:17], v[92:93]
	v_pk_mul_f32 v[34:35], v[2:3], s[2:3] op_sel_hi:[1,0]
	v_pk_mul_f32 v[38:39], v[10:11], s[2:3] op_sel_hi:[1,0]
	v_exp_f32_e32 v42, v42
	v_exp_f32_e32 v43, v43
	v_pk_mul_f32 v[40:41], v[16:17], s[2:3] op_sel_hi:[1,0]
	v_exp_f32_e32 v34, v34
	v_exp_f32_e32 v35, v35
	v_exp_f32_e32 v38, v38
	v_exp_f32_e32 v39, v39
	v_exp_f32_e32 v40, v40
	v_exp_f32_e32 v41, v41
	v_pk_mul_f32 v[4:5], v[4:5], v[108:109]
	v_pk_mul_f32 v[12:13], v[12:13], v[104:105]
	v_pk_mul_f32 v[0:1], v[0:1], v[32:33]
	v_pk_mul_f32 v[8:9], v[8:9], v[36:37]
	v_pk_mul_f32 v[0:1], v[4:5], v[0:1]
	v_pk_mul_f32 v[4:5], v[12:13], v[8:9]
	v_pk_add_f32 v[8:9], v[42:43], 1.0 op_sel_hi:[1,0]
	v_pk_add_f32 v[34:35], v[34:35], 1.0 op_sel_hi:[1,0]
	v_pk_add_f32 v[38:39], v[38:39], 1.0 op_sel_hi:[1,0]
	v_rcp_f32_e32 v8, v8
	v_rcp_f32_e32 v9, v9
	v_pk_add_f32 v[40:41], v[40:41], 1.0 op_sel_hi:[1,0]
	v_rcp_f32_e32 v34, v34
	v_rcp_f32_e32 v35, v35
	v_rcp_f32_e32 v38, v38
	v_rcp_f32_e32 v39, v39
	v_rcp_f32_e32 v40, v40
	v_rcp_f32_e32 v41, v41
	s_waitcnt vmcnt(2)
	v_pk_mul_f32 v[12:13], v[22:23], v[90:91]
	v_pk_mul_f32 v[8:9], v[18:19], v[8:9]
	v_pk_mul_f32 v[6:7], v[6:7], v[110:111]
	v_pk_mul_f32 v[14:15], v[14:15], v[106:107]
	v_pk_mul_f32 v[2:3], v[2:3], v[34:35]
	v_pk_mul_f32 v[10:11], v[10:11], v[38:39]
	v_pk_mul_f32 v[8:9], v[12:13], v[8:9]
	s_waitcnt vmcnt(1)
	v_pk_mul_f32 v[12:13], v[24:25], v[84:85]
	v_pk_mul_f32 v[20:21], v[20:21], v[88:89]
	v_pk_mul_f32 v[2:3], v[6:7], v[2:3]
	v_pk_mul_f32 v[6:7], v[14:15], v[10:11]
	v_pk_mul_f32 v[10:11], v[16:17], v[40:41]
	v_pk_mul_f32 v[16:17], v[12:13], s[2:3] op_sel_hi:[1,0]
	v_pk_mul_f32 v[18:19], v[26:27], v[86:87]
	v_pk_mul_f32 v[10:11], v[20:21], v[10:11]
	v_exp_f32_e32 v16, v16
	v_exp_f32_e32 v17, v17
	v_pk_mul_f32 v[20:21], v[18:19], s[2:3] op_sel_hi:[1,0]
	s_waitcnt vmcnt(0)
	v_pk_mul_f32 v[14:15], v[28:29], v[80:81]
	v_exp_f32_e32 v20, v20
	v_exp_f32_e32 v21, v21
	v_pk_add_f32 v[16:17], v[16:17], 1.0 op_sel_hi:[1,0]
	s_mov_b32 s3, 0x700000
	v_rcp_f32_e32 v16, v16
	v_rcp_f32_e32 v17, v17
	v_pk_add_f32 v[20:21], v[20:21], 1.0 op_sel_hi:[1,0]
	v_mov_b32_e32 v81, 0
	v_rcp_f32_e32 v20, v20
	v_rcp_f32_e32 v21, v21
	v_pk_mul_f32 v[12:13], v[12:13], v[16:17]
	v_pk_mul_f32 v[16:17], v[18:19], v[20:21]
	v_pk_mul_f32 v[12:13], v[14:15], v[12:13]
	v_pk_mul_f32 v[14:15], v[30:31], v[82:83]
	v_pk_mul_f32 v[14:15], v[14:15], v[16:17]
	v_max3_f32 v16, |v6|, |v7|, |v0|
	v_max3_f32 v16, v16, |v1|, |v2|
	v_max3_f32 v16, v16, |v3|, |v4|
	v_max3_f32 v16, v16, |v5|, |v10|
	v_max3_f32 v16, v16, |v11|, |v8|
	v_max3_f32 v16, v16, |v9|, |v12|
	v_max3_f32 v16, v16, |v13|, |v14|
	v_max_f32_e64 v16, v16, |v15|
	v_mov_b32_e32 v17, v16
	s_nop 1
	v_permlane16_swap_b32_e32 v16, v17
	v_max_f32_e32 v16, v16, v17
	v_lshrrev_b32_e32 v17, 23, v16
	v_and_b32_e32 v16, 0x7fffff, v16
	v_mov_b32_e32 v82, 0xffffff7f
	v_cmp_lt_u32_e32 vcc, s3, v16
	v_mov_b32_e32 v83, 0x64
	s_nop 0
	v_addc_co_u32_e32 v16, vcc, v17, v82, vcc
	v_med3_i32 v84, v16, s5, v83
	v_lshlrev_b32_e32 v16, 23, v84
	v_sub_u32_e32 v16, 1.0, v16
	v_pk_mul_f32 v[40:41], v[16:17], v[10:11] op_sel_hi:[0,1]
	v_pk_mul_f32 v[42:43], v[16:17], v[8:9] op_sel_hi:[0,1]
	v_pk_mul_f32 v[44:45], v[16:17], v[12:13] op_sel_hi:[0,1]
	v_pk_mul_f32 v[46:47], v[16:17], v[14:15] op_sel_hi:[0,1]
	v_pk_mul_f32 v[32:33], v[16:17], v[0:1] op_sel_hi:[0,1]
	v_pk_mul_f32 v[34:35], v[16:17], v[2:3] op_sel_hi:[0,1]
	v_pk_mul_f32 v[36:37], v[16:17], v[4:5] op_sel_hi:[0,1]
	v_pk_mul_f32 v[38:39], v[16:17], v[6:7] op_sel_hi:[0,1]
	v_cvt_scalef32_2xpk16_fp6_f32 v[86:91], v[32:47], v[40:55], 1.0
	v_cvt_scalef32_pk32_f32_fp6 v[0:31], v[86:91], s8
	v_fma_f32 v16, v32, s4, v0
	v_fma_f32 v17, v33, s4, v2
	v_fma_f32 v18, v34, s4, v4
	v_fma_f32 v19, v35, s4, v6
	v_fma_f32 v20, v36, s4, v8
	v_fma_f32 v21, v37, s4, v10
	v_fma_f32 v22, v38, s4, v12
	v_fma_f32 v23, v39, s4, v14
	v_fma_f32 v24, v40, s4, v1
	v_fma_f32 v25, v41, s4, v3
	v_fma_f32 v26, v42, s4, v5
	v_fma_f32 v27, v43, s4, v7
	v_fma_f32 v28, v44, s4, v9
	v_fma_f32 v29, v45, s4, v11
	v_fma_f32 v30, v46, s4, v13
	v_fma_f32 v31, v47, s4, v15
	v_cvt_scalef32_2xpk16_fp6_f32 v[0:5], v[16:31], v[24:39], 1.0
	v_xor_b32_e32 v4, 0x20820820, v0
	v_or_b32_e32 v0, 32, v163
	v_xor_b32_e32 v5, 0x8208208, v1
	v_or_b32_e32 v1, v0, v162
	v_mul_u32_u24_e32 v80, 24, v1
	v_xor_b32_e32 v6, 0x82082082, v2
	v_lshl_add_u64 v[2:3], v[148:149], 0, v[80:81]
	v_lshl_add_u64 v[2:3], v[2:3], 0, v[144:145]
	global_store_dwordx3 v[2:3], v[86:88], off nt
	v_add_co_u32_e32 v2, vcc, 0x1000, v2
	s_nop 1
	v_addc_co_u32_e32 v3, vcc, 0, v3, vcc
	global_store_dwordx3 v[2:3], v[4:6], off offset:2048 nt
	s_and_saveexec_b64 s[6:7], s[0:1]
	s_cbranch_execz .LBB2_12
	v_mov_b32_e32 v2, 0x7a00
	v_add_u32_e32 v1, 0x7f, v84
	v_lshl_add_u32 v2, v84, 8, v2
	v_lshl_or_b32 v80, v0, 1, v162
	v_or_b32_e32 v2, v2, v1
	v_lshl_add_u64 v[0:1], v[146:147], 0, v[80:81]
	global_store_short v[0:1], v2, off
.LBB2_12:
	s_or_b64 exec, exec, s[6:7]
	global_load_dwordx4 v[0:3], v[150:151], off
	global_load_dwordx4 v[4:7], v[152:153], off
	global_load_dwordx4 v[8:11], v[154:155], off offset:64
	global_load_dwordx4 v[12:15], v[156:157], off offset:64
	global_load_dwordx4 v[16:19], v[154:155], off offset:32
	global_load_dwordx4 v[20:23], v[156:157], off offset:32
	global_load_dwordx4 v[24:27], v[158:159], off offset:64
	global_load_dwordx4 v[28:31], v[160:161], off offset:64
	v_permlane32_swap_b32_e32 v68, v60
	v_permlane32_swap_b32_e32 v69, v61
	v_permlane32_swap_b32_e32 v64, v52
	v_permlane32_swap_b32_e32 v65, v53
	v_permlane32_swap_b32_e32 v70, v62
	v_permlane32_swap_b32_e32 v71, v63
	v_permlane32_swap_b32_e32 v66, v54
	v_permlane32_swap_b32_e32 v67, v55
	v_permlane32_swap_b32_e32 v76, v56
	v_permlane32_swap_b32_e32 v77, v57
	v_permlane32_swap_b32_e32 v72, v48
	v_permlane32_swap_b32_e32 v73, v49
	v_permlane32_swap_b32_e32 v78, v58
	v_permlane32_swap_b32_e32 v79, v59
	v_permlane32_swap_b32_e32 v74, v50
	v_permlane32_swap_b32_e32 v75, v51
	s_waitcnt vmcnt(7)
	v_pk_mul_f32 v[0:1], v[0:1], v[68:69]
	s_nop 0
	v_pk_mul_f32 v[32:33], v[0:1], s[2:3] op_sel_hi:[1,0]
	s_waitcnt vmcnt(5)
	v_pk_mul_f32 v[8:9], v[8:9], v[64:65]
	v_exp_f32_e32 v32, v32
	v_pk_mul_f32 v[36:37], v[8:9], s[2:3] op_sel_hi:[1,0]
	v_exp_f32_e32 v33, v33
	v_exp_f32_e32 v36, v36
	v_exp_f32_e32 v37, v37
	s_waitcnt vmcnt(3)
	v_pk_mul_f32 v[18:19], v[18:19], v[62:63]
	v_pk_mul_f32 v[2:3], v[2:3], v[70:71]
	v_pk_mul_f32 v[10:11], v[10:11], v[66:67]
	v_pk_mul_f32 v[42:43], v[18:19], s[2:3] op_sel_hi:[1,0]
	v_pk_add_f32 v[32:33], v[32:33], 1.0 op_sel_hi:[1,0]
	v_pk_add_f32 v[36:37], v[36:37], 1.0 op_sel_hi:[1,0]
	v_pk_mul_f32 v[16:17], v[16:17], v[60:61]
	v_pk_mul_f32 v[34:35], v[2:3], s[2:3] op_sel_hi:[1,0]
	v_pk_mul_f32 v[38:39], v[10:11], s[2:3] op_sel_hi:[1,0]
	v_exp_f32_e32 v42, v42
	v_exp_f32_e32 v43, v43
	v_rcp_f32_e32 v32, v32
	v_rcp_f32_e32 v33, v33
	v_rcp_f32_e32 v36, v36
	v_rcp_f32_e32 v37, v37
	v_pk_mul_f32 v[40:41], v[16:17], s[2:3] op_sel_hi:[1,0]
	v_exp_f32_e32 v34, v34
	v_exp_f32_e32 v35, v35
	v_exp_f32_e32 v38, v38
	v_exp_f32_e32 v39, v39
	v_exp_f32_e32 v40, v40
	v_exp_f32_e32 v41, v41
	v_pk_mul_f32 v[4:5], v[4:5], v[76:77]
	v_pk_mul_f32 v[12:13], v[12:13], v[72:73]
	v_pk_add_f32 v[42:43], v[42:43], 1.0 op_sel_hi:[1,0]
	v_pk_mul_f32 v[0:1], v[0:1], v[32:33]
	v_pk_mul_f32 v[8:9], v[8:9], v[36:37]
	v_pk_add_f32 v[34:35], v[34:35], 1.0 op_sel_hi:[1,0]
	v_pk_add_f32 v[38:39], v[38:39], 1.0 op_sel_hi:[1,0]
	v_pk_mul_f32 v[0:1], v[4:5], v[0:1]
	v_pk_mul_f32 v[4:5], v[12:13], v[8:9]
	v_rcp_f32_e32 v8, v42
	v_rcp_f32_e32 v9, v43
	v_pk_add_f32 v[40:41], v[40:41], 1.0 op_sel_hi:[1,0]
	v_rcp_f32_e32 v34, v34
	v_rcp_f32_e32 v35, v35
	v_rcp_f32_e32 v38, v38
	v_rcp_f32_e32 v39, v39
	v_rcp_f32_e32 v40, v40
	v_rcp_f32_e32 v41, v41
	s_waitcnt vmcnt(2)
	v_pk_mul_f32 v[12:13], v[22:23], v[58:59]
	v_pk_mul_f32 v[8:9], v[18:19], v[8:9]
	v_pk_mul_f32 v[6:7], v[6:7], v[78:79]
	v_pk_mul_f32 v[14:15], v[14:15], v[74:75]
	v_pk_mul_f32 v[2:3], v[2:3], v[34:35]
	v_pk_mul_f32 v[10:11], v[10:11], v[38:39]
	v_pk_mul_f32 v[8:9], v[12:13], v[8:9]
	s_waitcnt vmcnt(1)
	v_pk_mul_f32 v[12:13], v[24:25], v[52:53]
	v_pk_mul_f32 v[20:21], v[20:21], v[56:57]
	v_pk_mul_f32 v[2:3], v[6:7], v[2:3]
	v_pk_mul_f32 v[6:7], v[14:15], v[10:11]
	v_pk_mul_f32 v[10:11], v[16:17], v[40:41]
	v_pk_mul_f32 v[16:17], v[12:13], s[2:3] op_sel_hi:[1,0]
	v_pk_mul_f32 v[18:19], v[26:27], v[54:55]
	v_pk_mul_f32 v[10:11], v[20:21], v[10:11]
	v_exp_f32_e32 v16, v16
	v_exp_f32_e32 v17, v17
	v_pk_mul_f32 v[20:21], v[18:19], s[2:3] op_sel_hi:[1,0]
	s_waitcnt vmcnt(0)
	v_pk_mul_f32 v[14:15], v[28:29], v[48:49]
	v_exp_f32_e32 v20, v20
	v_exp_f32_e32 v21, v21
	v_pk_add_f32 v[16:17], v[16:17], 1.0 op_sel_hi:[1,0]
	v_pk_add_f32 v[20:21], v[20:21], 1.0 op_sel_hi:[1,0]
	v_rcp_f32_e32 v16, v16
	v_rcp_f32_e32 v17, v17
	v_rcp_f32_e32 v20, v20
	v_rcp_f32_e32 v21, v21
	v_pk_mul_f32 v[12:13], v[12:13], v[16:17]
	s_nop 0
	v_pk_mul_f32 v[12:13], v[14:15], v[12:13]
	v_pk_mul_f32 v[14:15], v[30:31], v[50:51]
	v_pk_mul_f32 v[16:17], v[18:19], v[20:21]
	v_pk_mul_f32 v[14:15], v[14:15], v[16:17]
	v_max3_f32 v16, |v6|, |v7|, |v0|
	v_max3_f32 v16, v16, |v1|, |v2|
	v_max3_f32 v16, v16, |v3|, |v4|
	v_max3_f32 v16, v16, |v5|, |v10|
	v_max3_f32 v16, v16, |v11|, |v8|
	v_max3_f32 v16, v16, |v9|, |v12|
	v_max3_f32 v16, v16, |v13|, |v14|
	v_max_f32_e64 v16, v16, |v15|
	v_mov_b32_e32 v17, v16
	s_nop 1
	v_permlane16_swap_b32_e32 v16, v17
	v_max_f32_e32 v16, v16, v17
	v_lshrrev_b32_e32 v17, 23, v16
	v_and_b32_e32 v16, 0x7fffff, v16
	v_cmp_lt_u32_e32 vcc, s3, v16
	s_nop 1
	v_addc_co_u32_e32 v16, vcc, v17, v82, vcc
	v_med3_i32 v48, v16, s5, v83
	v_lshlrev_b32_e32 v16, 23, v48
	v_sub_u32_e32 v16, 1.0, v16
	v_pk_mul_f32 v[40:41], v[16:17], v[10:11] op_sel_hi:[0,1]
	v_pk_mul_f32 v[42:43], v[16:17], v[8:9] op_sel_hi:[0,1]
	v_pk_mul_f32 v[44:45], v[16:17], v[12:13] op_sel_hi:[0,1]
	v_pk_mul_f32 v[46:47], v[16:17], v[14:15] op_sel_hi:[0,1]
	v_pk_mul_f32 v[32:33], v[16:17], v[0:1] op_sel_hi:[0,1]
	v_pk_mul_f32 v[34:35], v[16:17], v[2:3] op_sel_hi:[0,1]
	v_pk_mul_f32 v[36:37], v[16:17], v[4:5] op_sel_hi:[0,1]
	v_pk_mul_f32 v[38:39], v[16:17], v[6:7] op_sel_hi:[0,1]
	v_cvt_scalef32_2xpk16_fp6_f32 v[50:55], v[32:47], v[40:55], 1.0
	v_cvt_scalef32_pk32_f32_fp6 v[0:31], v[50:55], s8
	v_fma_f32 v16, v32, s4, v0
	v_fma_f32 v17, v33, s4, v2
	v_fma_f32 v18, v34, s4, v4
	v_fma_f32 v19, v35, s4, v6
	v_fma_f32 v20, v36, s4, v8
	v_fma_f32 v21, v37, s4, v10
	v_fma_f32 v22, v38, s4, v12
	v_fma_f32 v23, v39, s4, v14
	v_fma_f32 v24, v40, s4, v1
	v_fma_f32 v25, v41, s4, v3
	v_fma_f32 v26, v42, s4, v5
	v_fma_f32 v27, v43, s4, v7
	v_fma_f32 v28, v44, s4, v9
	v_fma_f32 v29, v45, s4, v11
	v_fma_f32 v30, v46, s4, v13
	v_fma_f32 v31, v47, s4, v15
	v_cvt_scalef32_2xpk16_fp6_f32 v[0:5], v[16:31], v[24:39], 1.0
	v_xor_b32_e32 v4, 0x20820820, v0
	v_or_b32_e32 v0, 48, v163
	v_xor_b32_e32 v5, 0x8208208, v1
	v_or_b32_e32 v1, v0, v162
	v_mul_u32_u24_e32 v80, 24, v1
	v_xor_b32_e32 v6, 0x82082082, v2
	v_lshl_add_u64 v[2:3], v[148:149], 0, v[80:81]
	v_lshl_add_u64 v[2:3], v[2:3], 0, v[144:145]
	global_store_dwordx3 v[2:3], v[50:52], off nt
	v_add_co_u32_e32 v2, vcc, 0x1000, v2
	s_nop 1
	v_addc_co_u32_e32 v3, vcc, 0, v3, vcc
	global_store_dwordx3 v[2:3], v[4:6], off offset:2048 nt
	s_and_saveexec_b64 s[2:3], s[0:1]
	s_cbranch_execz .LBB2_14
	v_mov_b32_e32 v2, 0x7a00
	v_add_u32_e32 v1, 0x7f, v48
	v_lshl_add_u32 v2, v48, 8, v2
	v_or_b32_e32 v2, v2, v1
	v_lshl_or_b32 v0, v0, 1, v162
	v_mov_b32_e32 v1, 0
	v_lshl_add_u64 v[0:1], v[146:147], 0, v[0:1]
	global_store_short v[0:1], v2, off

.LBB3_6:
	s_mov_b32 s0, 0
	s_ashr_i32 s1, s0, 31
	v_add_u32_e32 v26, s0, v0
	v_ashrrev_i32_e32 v0, 6, v26
	v_and_b32_e32 v0, -4, v0
	v_bfe_u32 v177, v26, 5, 1
	v_lshl_add_u32 v178, s12, 3, v0
	v_bfe_u32 v27, v26, 4, 1
	v_or_b32_e32 v0, v178, v177
	s_lshl_b64 s[4:5], s[0:1], 2
	v_lshlrev_b32_e32 v36, 5, v0
	v_lshlrev_b32_e32 v179, 2, v27
	s_add_u32 s4, s10, s4
	v_or_b32_e32 v30, v36, v179
	s_addc_u32 s5, s11, s5
	v_ashrrev_i32_e32 v31, 31, v30
	v_lshl_add_u64 v[170:171], v[30:31], 2, s[4:5]
	global_load_dwordx4 v[192:195], v[170:171], off
	v_ashrrev_i32_e32 v31, 31, v36
	v_lshl_add_u64 v[172:173], v[30:31], 2, s[4:5]
	global_load_dwordx4 v[196:199], v[172:173], off offset:64
	v_and_b32_e32 v181, 0xcf, v26
	v_mul_u32_u24_e32 v160, 12, v27
	v_cmp_eq_u32_e64 s[0:1], 0, v27
	global_load_dwordx4 v[200:203], v[172:173], off offset:32
	s_lshl_b32 s11, s8, 6
	v_ashrrev_i32_e32 v30, 1, v178
	v_or_b32_e32 v176, 8, v179
	v_add_u32_e32 v34, s11, v30
	s_movk_i32 s9, 0x6000
	v_mov_b64_e32 v[32:33], s[2:3]
	s_add_u32 s6, s2, 0x3000000
	v_ashrrev_i32_e32 v35, 31, v34
	v_or_b32_e32 v30, v36, v176
	s_addc_u32 s7, s3, 0
	v_mad_i64_i32 v[168:169], s[8:9], v34, s9, v[32:33]
	v_lshlrev_b64 v[32:33], 10, v[34:35]
	v_lshl_add_u64 v[174:175], v[30:31], 2, s[4:5]
	v_lshl_add_u64 v[166:167], s[6:7], 0, v[32:33]
	global_load_dwordx4 v[204:207], v[174:175], off offset:64
	global_load_dwordx4 v[208:211], v[170:171], off offset:256
	global_load_dwordx4 v[212:215], v[172:173], off offset:320
	global_load_dwordx4 v[216:219], v[172:173], off offset:288
	global_load_dwordx4 v[220:223], v[174:175], off offset:320
	v_permlane32_swap_b32_e32 v14, v6
	v_permlane32_swap_b32_e32 v15, v7
	v_permlane32_swap_b32_e32 v16, v8
	v_permlane32_swap_b32_e32 v17, v9
	v_permlane32_swap_b32_e32 v10, v2
	v_permlane32_swap_b32_e32 v11, v3
	s_mov_b32 s20, 0x3e6d3388
	s_mov_b32 s22, 0xbf3a00e3
	s_mov_b32 s16, 0x3f07dc22
	s_mov_b32 s14, 0xbf38aa3b
	v_mov_b64_e32 v[0:1], s[22:23]
	s_mov_b32 s18, 0x3f35f0e3
	s_mov_b32 s10, 0xbe11a98e
	s_mov_b32 s12, 0x3e027906
	v_permlane32_swap_b32_e32 v12, v4
	v_permlane32_swap_b32_e32 v13, v5
	s_mov_b32 s9, 0x700000
	v_mov_b32_e32 v182, 0xffffff7f
	v_mov_b32_e32 v183, 0x64
	s_mov_b32 s8, 0xc2000000
	v_lshlrev_b32_e32 v180, 9, v177
	v_mov_b32_e32 v161, 0
	v_mov_b32_e32 v165, v161
	v_lshl_or_b32 v162, v181, 1, v180
	s_waitcnt vmcnt(4)
	v_pk_mul_f32 v[14:15], v[192:193], v[14:15]
	s_nop 0
	v_and_b32_e32 v19, 0x7fffffff, v15
	v_and_b32_e32 v18, 0x7fffffff, v14
	v_pk_mul_f32 v[16:17], v[194:195], v[16:17]
	v_pk_mul_f32 v[10:11], v[196:197], v[10:11]
	v_pk_fma_f32 v[22:23], v[18:19], s[20:21], 1.0 op_sel_hi:[1,0,0]
	v_and_b32_e32 v35, 0x7fffffff, v17
	v_and_b32_e32 v34, 0x7fffffff, v16
	v_rcp_f32_e32 v22, v22
	v_rcp_f32_e32 v23, v23
	v_pk_fma_f32 v[38:39], v[34:35], s[20:21], 1.0 op_sel_hi:[1,0,0]
	v_pk_mul_f32 v[20:21], v[14:15], v[14:15]
	v_rcp_f32_e32 v38, v38
	v_rcp_f32_e32 v39, v39
	v_pk_mul_f32 v[20:21], v[20:21], s[14:15] op_sel_hi:[1,0]
	v_pk_fma_f32 v[44:45], v[22:23], s[16:17], v[0:1] op_sel_hi:[1,0,0]
	v_pk_mul_f32 v[36:37], v[16:17], v[16:17]
	v_exp_f32_e32 v20, v20
	v_exp_f32_e32 v21, v21
	v_pk_fma_f32 v[44:45], v[22:23], v[44:45], s[18:19] op_sel_hi:[1,1,0]
	v_pk_mul_f32 v[36:37], v[36:37], s[14:15] op_sel_hi:[1,0]
	v_pk_fma_f32 v[46:47], v[38:39], s[16:17], v[0:1] op_sel_hi:[1,0,0]
	v_pk_fma_f32 v[44:45], v[22:23], v[44:45], s[10:11] op_sel_hi:[1,1,0]
	v_and_b32_e32 v41, 0x7fffffff, v11
	v_and_b32_e32 v40, 0x7fffffff, v10
	v_exp_f32_e32 v36, v36
	v_exp_f32_e32 v37, v37
	v_pk_fma_f32 v[46:47], v[38:39], v[46:47], s[18:19] op_sel_hi:[1,1,0]
	v_pk_fma_f32 v[44:45], v[22:23], v[44:45], s[12:13] op_sel_hi:[1,1,0]
	v_pk_fma_f32 v[42:43], v[40:41], s[20:21], 1.0 op_sel_hi:[1,0,0]
	v_pk_fma_f32 v[46:47], v[38:39], v[46:47], s[10:11] op_sel_hi:[1,1,0]
	v_pk_mul_f32 v[22:23], v[22:23], v[44:45]
	v_rcp_f32_e32 v42, v42
	v_pk_fma_f32 v[46:47], v[38:39], v[46:47], s[12:13] op_sel_hi:[1,1,0]
	v_pk_fma_f32 v[20:21], v[20:21], v[22:23], 0.5 op_sel_hi:[1,1,0] neg_lo:[1,0,0] neg_hi:[1,0,0]
	v_rcp_f32_e32 v43, v43
	v_pk_mul_f32 v[38:39], v[38:39], v[46:47]
	v_pk_mul_f32 v[18:19], v[18:19], v[20:21]
	v_pk_mul_f32 v[20:21], v[10:11], v[10:11]
	v_pk_fma_f32 v[14:15], v[14:15], 0.5, v[18:19] op_sel_hi:[1,0,1]
	v_pk_fma_f32 v[18:19], v[36:37], v[38:39], 0.5 op_sel_hi:[1,1,0] neg_lo:[1,0,0] neg_hi:[1,0,0]
	v_pk_mul_f32 v[20:21], v[20:21], s[14:15] op_sel_hi:[1,0]
	v_pk_mul_f32 v[18:19], v[34:35], v[18:19]
	v_pk_mul_f32 v[12:13], v[198:199], v[12:13]
	v_pk_fma_f32 v[16:17], v[16:17], 0.5, v[18:19] op_sel_hi:[1,0,1]
	v_pk_fma_f32 v[18:19], v[42:43], s[16:17], v[0:1] op_sel_hi:[1,0,0]
	v_exp_f32_e32 v20, v20
	v_pk_fma_f32 v[18:19], v[42:43], v[18:19], s[18:19] op_sel_hi:[1,1,0]
	v_exp_f32_e32 v21, v21
	v_and_b32_e32 v23, 0x7fffffff, v13
	v_and_b32_e32 v22, 0x7fffffff, v12
	v_pk_fma_f32 v[18:19], v[42:43], v[18:19], s[10:11] op_sel_hi:[1,1,0]
	v_pk_fma_f32 v[24:25], v[22:23], s[20:21], 1.0 op_sel_hi:[1,0,0]
	v_pk_fma_f32 v[18:19], v[42:43], v[18:19], s[12:13] op_sel_hi:[1,1,0]
	v_rcp_f32_e32 v24, v24
	v_rcp_f32_e32 v25, v25
	v_pk_mul_f32 v[18:19], v[42:43], v[18:19]
	v_pk_mul_f32 v[6:7], v[200:201], v[6:7]
	v_pk_fma_f32 v[18:19], v[20:21], v[18:19], 0.5 op_sel_hi:[1,1,0] neg_lo:[1,0,0] neg_hi:[1,0,0]
	v_pk_mul_f32 v[20:21], v[12:13], v[12:13]
	v_pk_mul_f32 v[18:19], v[40:41], v[18:19]
	v_pk_mul_f32 v[20:21], v[20:21], s[14:15] op_sel_hi:[1,0]
	v_pk_fma_f32 v[10:11], v[10:11], 0.5, v[18:19] op_sel_hi:[1,0,1]
	v_pk_fma_f32 v[18:19], v[24:25], s[16:17], v[0:1] op_sel_hi:[1,0,0]
	v_exp_f32_e32 v20, v20
	v_pk_fma_f32 v[18:19], v[24:25], v[18:19], s[18:19] op_sel_hi:[1,1,0]
	v_exp_f32_e32 v21, v21
	v_pk_fma_f32 v[18:19], v[24:25], v[18:19], s[10:11] op_sel_hi:[1,1,0]
	v_pk_mul_f32 v[8:9], v[202:203], v[8:9]
	v_pk_fma_f32 v[18:19], v[24:25], v[18:19], s[12:13] op_sel_hi:[1,1,0]
	v_pk_mul_f32 v[2:3], v[204:205], v[2:3]
	v_pk_mul_f32 v[18:19], v[24:25], v[18:19]
	v_and_b32_e32 v25, 0x7fffffff, v7
	v_and_b32_e32 v24, 0x7fffffff, v6
	v_pk_fma_f32 v[26:27], v[24:25], s[20:21], 1.0 op_sel_hi:[1,0,0]
	v_pk_fma_f32 v[18:19], v[20:21], v[18:19], 0.5 op_sel_hi:[1,1,0] neg_lo:[1,0,0] neg_hi:[1,0,0]
	v_rcp_f32_e32 v26, v26
	v_rcp_f32_e32 v27, v27
	v_pk_mul_f32 v[18:19], v[22:23], v[18:19]
	v_pk_mul_f32 v[20:21], v[6:7], v[6:7]
	v_pk_fma_f32 v[12:13], v[12:13], 0.5, v[18:19] op_sel_hi:[1,0,1]
	v_pk_fma_f32 v[18:19], v[26:27], s[16:17], v[0:1] op_sel_hi:[1,0,0]
	v_pk_mul_f32 v[20:21], v[20:21], s[14:15] op_sel_hi:[1,0]
	v_pk_fma_f32 v[18:19], v[26:27], v[18:19], s[18:19] op_sel_hi:[1,1,0]
	v_exp_f32_e32 v20, v20
	v_pk_fma_f32 v[18:19], v[26:27], v[18:19], s[10:11] op_sel_hi:[1,1,0]
	v_exp_f32_e32 v21, v21
	v_pk_fma_f32 v[18:19], v[26:27], v[18:19], s[12:13] op_sel_hi:[1,1,0]
	v_and_b32_e32 v23, 0x7fffffff, v9
	v_and_b32_e32 v22, 0x7fffffff, v8
	v_pk_mul_f32 v[18:19], v[26:27], v[18:19]
	v_pk_fma_f32 v[26:27], v[22:23], s[20:21], 1.0 op_sel_hi:[1,0,0]
	v_pk_fma_f32 v[18:19], v[20:21], v[18:19], 0.5 op_sel_hi:[1,1,0] neg_lo:[1,0,0] neg_hi:[1,0,0]
	v_rcp_f32_e32 v26, v26
	v_rcp_f32_e32 v27, v27
	v_pk_mul_f32 v[18:19], v[24:25], v[18:19]
	v_pk_mul_f32 v[20:21], v[8:9], v[8:9]
	v_pk_fma_f32 v[6:7], v[6:7], 0.5, v[18:19] op_sel_hi:[1,0,1]
	v_pk_fma_f32 v[18:19], v[26:27], s[16:17], v[0:1] op_sel_hi:[1,0,0]
	v_pk_mul_f32 v[20:21], v[20:21], s[14:15] op_sel_hi:[1,0]
	v_pk_fma_f32 v[18:19], v[26:27], v[18:19], s[18:19] op_sel_hi:[1,1,0]
	v_exp_f32_e32 v20, v20
	v_pk_fma_f32 v[18:19], v[26:27], v[18:19], s[10:11] op_sel_hi:[1,1,0]
	v_exp_f32_e32 v21, v21
	v_pk_fma_f32 v[18:19], v[26:27], v[18:19], s[12:13] op_sel_hi:[1,1,0]
	v_and_b32_e32 v25, 0x7fffffff, v3
	v_and_b32_e32 v24, 0x7fffffff, v2
	v_pk_mul_f32 v[18:19], v[26:27], v[18:19]
	v_pk_fma_f32 v[26:27], v[24:25], s[20:21], 1.0 op_sel_hi:[1,0,0]
	v_pk_fma_f32 v[18:19], v[20:21], v[18:19], 0.5 op_sel_hi:[1,1,0] neg_lo:[1,0,0] neg_hi:[1,0,0]
	v_rcp_f32_e32 v26, v26
	v_rcp_f32_e32 v27, v27
	v_pk_mul_f32 v[18:19], v[22:23], v[18:19]
	v_pk_mul_f32 v[20:21], v[2:3], v[2:3]
	v_pk_fma_f32 v[8:9], v[8:9], 0.5, v[18:19] op_sel_hi:[1,0,1]
	v_pk_fma_f32 v[18:19], v[26:27], s[16:17], v[0:1] op_sel_hi:[1,0,0]
	v_pk_mul_f32 v[20:21], v[20:21], s[14:15] op_sel_hi:[1,0]
	v_pk_fma_f32 v[18:19], v[26:27], v[18:19], s[18:19] op_sel_hi:[1,1,0]
	v_exp_f32_e32 v20, v20
	v_pk_fma_f32 v[18:19], v[26:27], v[18:19], s[10:11] op_sel_hi:[1,1,0]
	v_exp_f32_e32 v21, v21
	v_pk_mul_f32 v[4:5], v[206:207], v[4:5]
	v_pk_fma_f32 v[18:19], v[26:27], v[18:19], s[12:13] op_sel_hi:[1,1,0]
	v_and_b32_e32 v23, 0x7fffffff, v5
	v_and_b32_e32 v22, 0x7fffffff, v4
	v_pk_mul_f32 v[18:19], v[26:27], v[18:19]
	v_pk_fma_f32 v[26:27], v[22:23], s[20:21], 1.0 op_sel_hi:[1,0,0]
	v_pk_fma_f32 v[18:19], v[20:21], v[18:19], 0.5 op_sel_hi:[1,1,0] neg_lo:[1,0,0] neg_hi:[1,0,0]
	v_rcp_f32_e32 v26, v26
	v_rcp_f32_e32 v27, v27
	v_pk_mul_f32 v[18:19], v[24:25], v[18:19]
	v_pk_fma_f32 v[0:1], v[26:27], s[16:17], v[0:1] op_sel_hi:[1,0,0]
	v_pk_fma_f32 v[2:3], v[2:3], 0.5, v[18:19] op_sel_hi:[1,0,1]
	v_pk_mul_f32 v[18:19], v[4:5], v[4:5]
	v_pk_fma_f32 v[0:1], v[26:27], v[0:1], s[18:19] op_sel_hi:[1,1,0]
	v_pk_mul_f32 v[18:19], v[18:19], s[14:15] op_sel_hi:[1,0]
	v_pk_fma_f32 v[0:1], v[26:27], v[0:1], s[10:11] op_sel_hi:[1,1,0]
	v_exp_f32_e32 v18, v18
	v_exp_f32_e32 v19, v19
	v_pk_fma_f32 v[0:1], v[26:27], v[0:1], s[12:13] op_sel_hi:[1,1,0]
	s_movk_i32 s13, 0xff9c
	v_pk_mul_f32 v[0:1], v[26:27], v[0:1]
	s_mov_b32 s15, 0x42000000
	v_pk_fma_f32 v[0:1], v[18:19], v[0:1], 0.5 op_sel_hi:[1,1,0] neg_lo:[1,0,0] neg_hi:[1,0,0]
	v_pk_mul_f32 v[0:1], v[22:23], v[0:1]
	s_nop 0
	v_pk_fma_f32 v[0:1], v[4:5], 0.5, v[0:1] op_sel_hi:[1,0,1]
	v_max3_f32 v4, |v12|, |v13|, |v14|
	v_max3_f32 v4, v4, |v15|, |v16|
	v_max3_f32 v4, v4, |v17|, |v10|
	v_max3_f32 v4, v4, |v11|, |v6|
	v_max3_f32 v4, v4, |v7|, |v8|
	v_max3_f32 v4, v4, |v9|, |v2|
	v_max3_f32 v4, v4, |v3|, |v0|
	v_max_f32_e64 v4, v4, |v1|
	v_mov_b32_e32 v5, v4
	s_nop 1
	v_permlane16_swap_b32_e32 v4, v5
	v_max_f32_e32 v4, v4, v5
	v_lshrrev_b32_e32 v5, 23, v4
	v_and_b32_e32 v4, 0x7fffff, v4
	v_cmp_lt_u32_e32 vcc, s9, v4
	s_nop 1
	v_addc_co_u32_e32 v4, vcc, v5, v182, vcc
	v_med3_i32 v163, v4, s13, v183
	v_lshlrev_b32_e32 v4, 23, v163
	v_sub_u32_e32 v4, 1.0, v4
	v_pk_mul_f32 v[40:41], v[4:5], v[6:7] op_sel_hi:[0,1]
	v_pk_mul_f32 v[42:43], v[4:5], v[8:9] op_sel_hi:[0,1]
	v_pk_mul_f32 v[44:45], v[4:5], v[2:3] op_sel_hi:[0,1]
	v_pk_mul_f32 v[46:47], v[4:5], v[0:1] op_sel_hi:[0,1]
	v_pk_mul_f32 v[32:33], v[4:5], v[14:15] op_sel_hi:[0,1]
	v_pk_mul_f32 v[34:35], v[4:5], v[16:17] op_sel_hi:[0,1]
	v_pk_mul_f32 v[36:37], v[4:5], v[10:11] op_sel_hi:[0,1]
	v_pk_mul_f32 v[38:39], v[4:5], v[12:13] op_sel_hi:[0,1]
	v_cvt_scalef32_2xpk16_fp6_f32 v[184:189], v[32:47], v[40:55], 1.0
	v_cvt_scalef32_pk32_f32_fp6 v[0:31], v[184:189], s15
	v_fma_f32 v16, v32, s8, v0
	v_fma_f32 v17, v33, s8, v2
	v_fma_f32 v18, v34, s8, v4
	v_fma_f32 v19, v35, s8, v6
	v_fma_f32 v20, v36, s8, v8
	v_fma_f32 v21, v37, s8, v10
	v_fma_f32 v22, v38, s8, v12
	v_fma_f32 v23, v39, s8, v14
	v_fma_f32 v24, v40, s8, v1
	v_fma_f32 v25, v41, s8, v3
	v_fma_f32 v26, v42, s8, v5
	v_fma_f32 v27, v43, s8, v7
	v_fma_f32 v28, v44, s8, v9
	v_fma_f32 v29, v45, s8, v11
	v_fma_f32 v30, v46, s8, v13
	v_fma_f32 v31, v47, s8, v15
	v_cvt_scalef32_2xpk16_fp6_f32 v[0:5], v[16:31], v[24:39], 1.0
	v_or_b32_e32 v3, v181, v180
	v_mul_u32_u24_e32 v164, 24, v3
	v_lshl_add_u64 v[4:5], v[168:169], 0, v[164:165]
	v_lshl_add_u64 v[4:5], v[4:5], 0, v[160:161]
	global_store_dwordx3 v[4:5], v[184:186], off nt
	v_add_co_u32_e32 v4, vcc, 0x1000, v4
	v_xor_b32_e32 v0, 0x20820820, v0
	v_xor_b32_e32 v1, 0x8208208, v1
	v_xor_b32_e32 v2, 0x82082082, v2
	v_addc_co_u32_e32 v5, vcc, 0, v5, vcc
	global_store_dwordx3 v[4:5], v[0:2], off offset:2048 nt
	s_and_saveexec_b64 s[24:25], s[0:1]
	s_cbranch_execz .LBB3_8
	v_mov_b32_e32 v1, 0x7a00
	v_add_u32_e32 v0, 0x7f, v163
	v_lshl_add_u32 v1, v163, 8, v1
	v_mov_b32_e32 v163, v161
	v_or_b32_e32 v2, v1, v0
	v_lshl_add_u64 v[0:1], v[166:167], 0, v[162:163]
	global_store_short v[0:1], v2, off
.LBB3_8:
	s_or_b64 exec, exec, s[24:25]
	v_permlane32_swap_b32_e32 v156, v148
	v_permlane32_swap_b32_e32 v157, v149
	v_permlane32_swap_b32_e32 v158, v150
	v_permlane32_swap_b32_e32 v159, v151
	v_permlane32_swap_b32_e32 v154, v146
	v_permlane32_swap_b32_e32 v155, v147
	v_permlane32_swap_b32_e32 v152, v144
	v_permlane32_swap_b32_e32 v153, v145
	v_mov_b64_e32 v[16:17], s[22:23]
	v_pk_mul_f32 v[0:1], v[192:193], v[156:157]
	v_pk_mul_f32 v[2:3], v[194:195], v[158:159]
	v_and_b32_e32 v19, 0x7fffffff, v1
	v_and_b32_e32 v18, 0x7fffffff, v0
	v_pk_mul_f32 v[6:7], v[198:199], v[154:155]
	v_and_b32_e32 v23, 0x7fffffff, v3
	v_and_b32_e32 v22, 0x7fffffff, v2
	v_pk_fma_f32 v[36:37], v[18:19], s[20:21], 1.0 op_sel_hi:[1,0,0]
	v_pk_mul_f32 v[4:5], v[196:197], v[152:153]
	v_and_b32_e32 v31, 0x7fffffff, v7
	v_and_b32_e32 v30, 0x7fffffff, v6
	v_pk_fma_f32 v[38:39], v[22:23], s[20:21], 1.0 op_sel_hi:[1,0,0]
	v_rcp_f32_e32 v36, v36
	v_rcp_f32_e32 v37, v37
	v_and_b32_e32 v27, 0x7fffffff, v5
	v_and_b32_e32 v26, 0x7fffffff, v4
	v_pk_fma_f32 v[42:43], v[30:31], s[20:21], 1.0 op_sel_hi:[1,0,0]
	v_rcp_f32_e32 v38, v38
	v_rcp_f32_e32 v39, v39
	v_pk_fma_f32 v[40:41], v[26:27], s[20:21], 1.0 op_sel_hi:[1,0,0]
	v_rcp_f32_e32 v42, v42
	v_rcp_f32_e32 v43, v43
	v_pk_mul_f32 v[20:21], v[0:1], v[0:1]
	v_rcp_f32_e32 v40, v40
	v_rcp_f32_e32 v41, v41
	v_pk_mul_f32 v[24:25], v[2:3], v[2:3]
	v_pk_mul_f32 v[20:21], v[20:21], s[14:15] op_sel_hi:[1,0]
	v_pk_fma_f32 v[46:47], v[36:37], s[16:17], v[16:17] op_sel_hi:[1,0,0]
	v_pk_mul_f32 v[8:9], v[200:201], v[148:149]
	v_pk_mul_f32 v[32:33], v[6:7], v[6:7]
	v_pk_mul_f32 v[24:25], v[24:25], s[14:15] op_sel_hi:[1,0]
	v_exp_f32_e32 v20, v20
	v_exp_f32_e32 v21, v21
	v_pk_fma_f32 v[148:149], v[38:39], s[16:17], v[16:17] op_sel_hi:[1,0,0]
	v_pk_fma_f32 v[46:47], v[36:37], v[46:47], s[18:19] op_sel_hi:[1,1,0]
	v_pk_mul_f32 v[28:29], v[4:5], v[4:5]
	v_pk_mul_f32 v[32:33], v[32:33], s[14:15] op_sel_hi:[1,0]
	v_exp_f32_e32 v24, v24
	v_exp_f32_e32 v25, v25
	v_pk_fma_f32 v[154:155], v[42:43], s[16:17], v[16:17] op_sel_hi:[1,0,0]
	v_pk_fma_f32 v[148:149], v[38:39], v[148:149], s[18:19] op_sel_hi:[1,1,0]
	v_pk_fma_f32 v[46:47], v[36:37], v[46:47], s[10:11] op_sel_hi:[1,1,0]
	v_and_b32_e32 v35, 0x7fffffff, v9
	v_and_b32_e32 v34, 0x7fffffff, v8
	v_pk_mul_f32 v[28:29], v[28:29], s[14:15] op_sel_hi:[1,0]
	v_exp_f32_e32 v32, v32
	v_exp_f32_e32 v33, v33
	v_pk_fma_f32 v[152:153], v[40:41], s[16:17], v[16:17] op_sel_hi:[1,0,0]
	v_pk_fma_f32 v[154:155], v[42:43], v[154:155], s[18:19] op_sel_hi:[1,1,0]
	v_pk_fma_f32 v[148:149], v[38:39], v[148:149], s[10:11] op_sel_hi:[1,1,0]
	v_pk_fma_f32 v[46:47], v[36:37], v[46:47], s[12:13] op_sel_hi:[1,1,0]
	v_pk_fma_f32 v[44:45], v[34:35], s[20:21], 1.0 op_sel_hi:[1,0,0]
	v_exp_f32_e32 v28, v28
	v_exp_f32_e32 v29, v29
	v_pk_fma_f32 v[152:153], v[40:41], v[152:153], s[18:19] op_sel_hi:[1,1,0]
	v_pk_fma_f32 v[154:155], v[42:43], v[154:155], s[10:11] op_sel_hi:[1,1,0]
	v_pk_fma_f32 v[148:149], v[38:39], v[148:149], s[12:13] op_sel_hi:[1,1,0]
	v_pk_mul_f32 v[36:37], v[36:37], v[46:47]
	v_rcp_f32_e32 v44, v44
	v_pk_fma_f32 v[152:153], v[40:41], v[152:153], s[10:11] op_sel_hi:[1,1,0]
	v_pk_fma_f32 v[154:155], v[42:43], v[154:155], s[12:13] op_sel_hi:[1,1,0]
	v_pk_mul_f32 v[38:39], v[38:39], v[148:149]
	v_pk_fma_f32 v[20:21], v[20:21], v[36:37], 0.5 op_sel_hi:[1,1,0] neg_lo:[1,0,0] neg_hi:[1,0,0]
	v_rcp_f32_e32 v45, v45
	v_pk_fma_f32 v[152:153], v[40:41], v[152:153], s[12:13] op_sel_hi:[1,1,0]
	v_pk_mul_f32 v[42:43], v[42:43], v[154:155]
	v_pk_fma_f32 v[24:25], v[24:25], v[38:39], 0.5 op_sel_hi:[1,1,0] neg_lo:[1,0,0] neg_hi:[1,0,0]
	v_pk_mul_f32 v[18:19], v[18:19], v[20:21]
	v_pk_mul_f32 v[40:41], v[40:41], v[152:153]
	v_pk_mul_f32 v[20:21], v[22:23], v[24:25]
	v_pk_fma_f32 v[0:1], v[0:1], 0.5, v[18:19] op_sel_hi:[1,0,1]
	v_pk_fma_f32 v[18:19], v[32:33], v[42:43], 0.5 op_sel_hi:[1,1,0] neg_lo:[1,0,0] neg_hi:[1,0,0]
	v_pk_fma_f32 v[28:29], v[28:29], v[40:41], 0.5 op_sel_hi:[1,1,0] neg_lo:[1,0,0] neg_hi:[1,0,0]
	v_pk_fma_f32 v[2:3], v[2:3], 0.5, v[20:21] op_sel_hi:[1,0,1]
	v_pk_mul_f32 v[18:19], v[30:31], v[18:19]
	v_pk_mul_f32 v[20:21], v[8:9], v[8:9]
	v_pk_mul_f32 v[22:23], v[26:27], v[28:29]
	v_pk_fma_f32 v[6:7], v[6:7], 0.5, v[18:19] op_sel_hi:[1,0,1]
	v_pk_fma_f32 v[18:19], v[44:45], s[16:17], v[16:17] op_sel_hi:[1,0,0]
	v_pk_mul_f32 v[20:21], v[20:21], s[14:15] op_sel_hi:[1,0]
	v_pk_mul_f32 v[10:11], v[202:203], v[150:151]
	v_pk_fma_f32 v[4:5], v[4:5], 0.5, v[22:23] op_sel_hi:[1,0,1]
	v_pk_fma_f32 v[18:19], v[44:45], v[18:19], s[18:19] op_sel_hi:[1,1,0]
	v_exp_f32_e32 v20, v20
	v_exp_f32_e32 v21, v21
	v_and_b32_e32 v23, 0x7fffffff, v11
	v_and_b32_e32 v22, 0x7fffffff, v10
	v_pk_fma_f32 v[18:19], v[44:45], v[18:19], s[10:11] op_sel_hi:[1,1,0]
	v_pk_fma_f32 v[24:25], v[22:23], s[20:21], 1.0 op_sel_hi:[1,0,0]
	v_pk_fma_f32 v[18:19], v[44:45], v[18:19], s[12:13] op_sel_hi:[1,1,0]
	v_rcp_f32_e32 v24, v24
	v_rcp_f32_e32 v25, v25
	v_pk_mul_f32 v[18:19], v[44:45], v[18:19]
	v_pk_mul_f32 v[12:13], v[204:205], v[144:145]
	v_pk_fma_f32 v[18:19], v[20:21], v[18:19], 0.5 op_sel_hi:[1,1,0] neg_lo:[1,0,0] neg_hi:[1,0,0]
	v_pk_mul_f32 v[20:21], v[10:11], v[10:11]
	v_pk_mul_f32 v[18:19], v[34:35], v[18:19]
	v_pk_mul_f32 v[20:21], v[20:21], s[14:15] op_sel_hi:[1,0]
	v_pk_fma_f32 v[8:9], v[8:9], 0.5, v[18:19] op_sel_hi:[1,0,1]
	v_pk_fma_f32 v[18:19], v[24:25], s[16:17], v[16:17] op_sel_hi:[1,0,0]
	v_exp_f32_e32 v20, v20
	v_pk_fma_f32 v[18:19], v[24:25], v[18:19], s[18:19] op_sel_hi:[1,1,0]
	v_exp_f32_e32 v21, v21
	v_pk_fma_f32 v[18:19], v[24:25], v[18:19], s[10:11] op_sel_hi:[1,1,0]
	v_pk_mul_f32 v[14:15], v[206:207], v[146:147]
	v_pk_fma_f32 v[18:19], v[24:25], v[18:19], s[12:13] op_sel_hi:[1,1,0]
	v_mov_b32_e32 v147, v161
	v_pk_mul_f32 v[18:19], v[24:25], v[18:19]
	v_and_b32_e32 v25, 0x7fffffff, v13
	v_and_b32_e32 v24, 0x7fffffff, v12
	v_pk_fma_f32 v[26:27], v[24:25], s[20:21], 1.0 op_sel_hi:[1,0,0]
	v_pk_fma_f32 v[18:19], v[20:21], v[18:19], 0.5 op_sel_hi:[1,1,0] neg_lo:[1,0,0] neg_hi:[1,0,0]
	v_rcp_f32_e32 v26, v26
	v_rcp_f32_e32 v27, v27
	v_pk_mul_f32 v[18:19], v[22:23], v[18:19]
	v_pk_mul_f32 v[20:21], v[12:13], v[12:13]
	v_pk_fma_f32 v[10:11], v[10:11], 0.5, v[18:19] op_sel_hi:[1,0,1]
	v_pk_fma_f32 v[18:19], v[26:27], s[16:17], v[16:17] op_sel_hi:[1,0,0]
	v_pk_mul_f32 v[20:21], v[20:21], s[14:15] op_sel_hi:[1,0]
	v_pk_fma_f32 v[18:19], v[26:27], v[18:19], s[18:19] op_sel_hi:[1,1,0]
	v_exp_f32_e32 v20, v20
	v_pk_fma_f32 v[18:19], v[26:27], v[18:19], s[10:11] op_sel_hi:[1,1,0]
	v_exp_f32_e32 v21, v21
	v_pk_fma_f32 v[18:19], v[26:27], v[18:19], s[12:13] op_sel_hi:[1,1,0]
	v_and_b32_e32 v23, 0x7fffffff, v15
	v_and_b32_e32 v22, 0x7fffffff, v14
	v_pk_mul_f32 v[18:19], v[26:27], v[18:19]
	v_pk_fma_f32 v[26:27], v[22:23], s[20:21], 1.0 op_sel_hi:[1,0,0]
	v_pk_fma_f32 v[18:19], v[20:21], v[18:19], 0.5 op_sel_hi:[1,1,0] neg_lo:[1,0,0] neg_hi:[1,0,0]
	v_rcp_f32_e32 v26, v26
	v_rcp_f32_e32 v27, v27
	v_pk_mul_f32 v[18:19], v[24:25], v[18:19]
	v_pk_fma_f32 v[16:17], v[26:27], s[16:17], v[16:17] op_sel_hi:[1,0,0]
	v_pk_fma_f32 v[12:13], v[12:13], 0.5, v[18:19] op_sel_hi:[1,0,1]
	v_pk_mul_f32 v[18:19], v[14:15], v[14:15]
	v_pk_fma_f32 v[16:17], v[26:27], v[16:17], s[18:19] op_sel_hi:[1,1,0]
	v_pk_mul_f32 v[18:19], v[18:19], s[14:15] op_sel_hi:[1,0]
	v_pk_fma_f32 v[16:17], v[26:27], v[16:17], s[10:11] op_sel_hi:[1,1,0]
	v_exp_f32_e32 v18, v18
	v_exp_f32_e32 v19, v19
	v_pk_fma_f32 v[16:17], v[26:27], v[16:17], s[12:13] op_sel_hi:[1,1,0]
	s_nop 0
	v_pk_mul_f32 v[16:17], v[26:27], v[16:17]
	s_nop 0
	v_pk_fma_f32 v[16:17], v[18:19], v[16:17], 0.5 op_sel_hi:[1,1,0] neg_lo:[1,0,0] neg_hi:[1,0,0]
	v_pk_mul_f32 v[16:17], v[22:23], v[16:17]
	s_nop 0
	v_pk_fma_f32 v[14:15], v[14:15], 0.5, v[16:17] op_sel_hi:[1,0,1]
	v_max3_f32 v16, |v6|, |v7|, |v0|
	v_max3_f32 v16, v16, |v1|, |v2|
	v_max3_f32 v16, v16, |v3|, |v4|
	v_max3_f32 v16, v16, |v5|, |v8|
	v_max3_f32 v16, v16, |v9|, |v10|
	v_max3_f32 v16, v16, |v11|, |v12|
	v_max3_f32 v16, v16, |v13|, |v14|
	v_max_f32_e64 v16, v16, |v15|
	v_mov_b32_e32 v17, v16
	s_nop 1
	v_permlane16_swap_b32_e32 v16, v17
	v_max_f32_e32 v16, v16, v17
	v_lshrrev_b32_e32 v17, 23, v16
	v_and_b32_e32 v16, 0x7fffff, v16
	v_cmp_lt_u32_e32 vcc, s9, v16
	s_nop 1
	v_addc_co_u32_e32 v16, vcc, v17, v182, vcc
	v_med3_i32 v145, v16, s13, v183
	v_lshlrev_b32_e32 v16, 23, v145
	v_sub_u32_e32 v16, 1.0, v16
	v_pk_mul_f32 v[40:41], v[16:17], v[8:9] op_sel_hi:[0,1]
	v_pk_mul_f32 v[42:43], v[16:17], v[10:11] op_sel_hi:[0,1]
	v_pk_mul_f32 v[44:45], v[16:17], v[12:13] op_sel_hi:[0,1]
	v_pk_mul_f32 v[46:47], v[16:17], v[14:15] op_sel_hi:[0,1]
	v_pk_mul_f32 v[32:33], v[16:17], v[0:1] op_sel_hi:[0,1]
	v_pk_mul_f32 v[34:35], v[16:17], v[2:3] op_sel_hi:[0,1]
	v_pk_mul_f32 v[36:37], v[16:17], v[4:5] op_sel_hi:[0,1]
	v_pk_mul_f32 v[38:39], v[16:17], v[6:7] op_sel_hi:[0,1]
	v_cvt_scalef32_2xpk16_fp6_f32 v[148:153], v[32:47], v[40:55], 1.0
	v_cvt_scalef32_pk32_f32_fp6 v[0:31], v[148:153], s15
	v_fma_f32 v16, v32, s8, v0
	v_fma_f32 v17, v33, s8, v2
	v_fma_f32 v18, v34, s8, v4
	v_fma_f32 v19, v35, s8, v6
	v_fma_f32 v20, v36, s8, v8
	v_fma_f32 v21, v37, s8, v10
	v_fma_f32 v22, v38, s8, v12
	v_fma_f32 v23, v39, s8, v14
	v_fma_f32 v24, v40, s8, v1
	v_fma_f32 v25, v41, s8, v3
	v_fma_f32 v26, v42, s8, v5
	v_fma_f32 v27, v43, s8, v7
	v_fma_f32 v28, v44, s8, v9
	v_fma_f32 v29, v45, s8, v11
	v_fma_f32 v30, v46, s8, v13
	v_fma_f32 v31, v47, s8, v15
	v_cvt_scalef32_2xpk16_fp6_f32 v[0:5], v[16:31], v[24:39], 1.0
	v_or_b32_e32 v3, 16, v181
	v_or_b32_e32 v4, v3, v180
	v_mul_u32_u24_e32 v146, 24, v4
	v_lshl_add_u64 v[4:5], v[168:169], 0, v[146:147]
	v_lshl_add_u64 v[4:5], v[4:5], 0, v[160:161]
	global_store_dwordx3 v[4:5], v[148:150], off nt
	v_add_co_u32_e32 v4, vcc, 0x1000, v4
	v_xor_b32_e32 v0, 0x20820820, v0
	v_xor_b32_e32 v1, 0x8208208, v1
	v_xor_b32_e32 v2, 0x82082082, v2
	v_addc_co_u32_e32 v5, vcc, 0, v5, vcc
	v_lshl_or_b32 v144, v3, 1, v180
	global_store_dwordx3 v[4:5], v[0:2], off offset:2048 nt
	s_and_saveexec_b64 s[8:9], s[0:1]
	s_cbranch_execz .LBB3_10
	v_mov_b32_e32 v1, 0x7a00
	v_add_u32_e32 v0, 0x7f, v145
	v_lshl_add_u32 v1, v145, 8, v1
	v_mov_b32_e32 v145, 0
	v_or_b32_e32 v2, v1, v0
	v_lshl_add_u64 v[0:1], v[166:167], 0, v[144:145]
	global_store_short v[0:1], v2, off
.LBB3_10:
	s_or_b64 exec, exec, s[8:9]
	v_permlane32_swap_b32_e32 v140, v132
	v_permlane32_swap_b32_e32 v141, v133
	v_permlane32_swap_b32_e32 v142, v134
	v_permlane32_swap_b32_e32 v143, v135
	v_permlane32_swap_b32_e32 v136, v128
	v_permlane32_swap_b32_e32 v137, v129
	s_mov_b32 s18, 0x3e6d3388
	v_permlane32_swap_b32_e32 v138, v130
	v_permlane32_swap_b32_e32 v139, v131
	s_mov_b32 s14, 0x3f07dc22
	s_mov_b32 s12, 0xbf38aa3b
	v_mov_b64_e32 v[16:17], s[22:23]
	s_mov_b32 s16, 0x3f35f0e3
	s_mov_b32 s8, 0xbe11a98e
	s_mov_b32 s10, 0x3e027906
	s_mov_b32 s20, 0xc2000000
	v_pk_mul_f32 v[0:1], v[192:193], v[140:141]
	v_pk_mul_f32 v[2:3], v[194:195], v[142:143]
	v_pk_mul_f32 v[4:5], v[196:197], v[136:137]
	v_and_b32_e32 v19, 0x7fffffff, v1
	v_and_b32_e32 v18, 0x7fffffff, v0
	v_and_b32_e32 v23, 0x7fffffff, v3
	v_and_b32_e32 v22, 0x7fffffff, v2
	v_and_b32_e32 v27, 0x7fffffff, v5
	v_and_b32_e32 v26, 0x7fffffff, v4
	v_pk_fma_f32 v[34:35], v[18:19], s[18:19], 1.0 op_sel_hi:[1,0,0]
	v_pk_fma_f32 v[36:37], v[22:23], s[18:19], 1.0 op_sel_hi:[1,0,0]
	v_pk_fma_f32 v[38:39], v[26:27], s[18:19], 1.0 op_sel_hi:[1,0,0]
	v_rcp_f32_e32 v34, v34
	v_rcp_f32_e32 v35, v35
	v_rcp_f32_e32 v36, v36
	v_rcp_f32_e32 v37, v37
	v_rcp_f32_e32 v38, v38
	v_rcp_f32_e32 v39, v39
	v_pk_mul_f32 v[6:7], v[198:199], v[138:139]
	v_pk_mul_f32 v[20:21], v[0:1], v[0:1]
	v_pk_mul_f32 v[24:25], v[2:3], v[2:3]
	v_pk_mul_f32 v[28:29], v[4:5], v[4:5]
	v_and_b32_e32 v31, 0x7fffffff, v7
	v_and_b32_e32 v30, 0x7fffffff, v6
	v_pk_mul_f32 v[20:21], v[20:21], s[12:13] op_sel_hi:[1,0]
	v_pk_mul_f32 v[24:25], v[24:25], s[12:13] op_sel_hi:[1,0]
	v_pk_fma_f32 v[42:43], v[34:35], s[14:15], v[16:17] op_sel_hi:[1,0,0]
	v_pk_fma_f32 v[44:45], v[36:37], s[14:15], v[16:17] op_sel_hi:[1,0,0]
	v_pk_mul_f32 v[28:29], v[28:29], s[12:13] op_sel_hi:[1,0]
	v_pk_fma_f32 v[40:41], v[30:31], s[18:19], 1.0 op_sel_hi:[1,0,0]
	v_exp_f32_e32 v20, v20
	v_exp_f32_e32 v21, v21
	v_exp_f32_e32 v24, v24
	v_exp_f32_e32 v25, v25
	v_pk_fma_f32 v[46:47], v[38:39], s[14:15], v[16:17] op_sel_hi:[1,0,0]
	v_pk_fma_f32 v[42:43], v[34:35], v[42:43], s[16:17] op_sel_hi:[1,1,0]
	v_pk_fma_f32 v[44:45], v[36:37], v[44:45], s[16:17] op_sel_hi:[1,1,0]
	v_exp_f32_e32 v28, v28
	v_exp_f32_e32 v29, v29
	v_rcp_f32_e32 v40, v40
	v_rcp_f32_e32 v41, v41
	v_pk_fma_f32 v[46:47], v[38:39], v[46:47], s[16:17] op_sel_hi:[1,1,0]
	v_pk_fma_f32 v[42:43], v[34:35], v[42:43], s[8:9] op_sel_hi:[1,1,0]
	v_pk_fma_f32 v[44:45], v[36:37], v[44:45], s[8:9] op_sel_hi:[1,1,0]
	v_pk_fma_f32 v[46:47], v[38:39], v[46:47], s[8:9] op_sel_hi:[1,1,0]
	v_pk_fma_f32 v[42:43], v[34:35], v[42:43], s[10:11] op_sel_hi:[1,1,0]
	v_pk_fma_f32 v[44:45], v[36:37], v[44:45], s[10:11] op_sel_hi:[1,1,0]
	v_pk_fma_f32 v[46:47], v[38:39], v[46:47], s[10:11] op_sel_hi:[1,1,0]
	v_pk_mul_f32 v[34:35], v[34:35], v[42:43]
	v_pk_mul_f32 v[36:37], v[36:37], v[44:45]
	v_pk_mul_f32 v[32:33], v[6:7], v[6:7]
	v_pk_mul_f32 v[38:39], v[38:39], v[46:47]
	v_pk_fma_f32 v[20:21], v[20:21], v[34:35], 0.5 op_sel_hi:[1,1,0] neg_lo:[1,0,0] neg_hi:[1,0,0]
	v_pk_fma_f32 v[24:25], v[24:25], v[36:37], 0.5 op_sel_hi:[1,1,0] neg_lo:[1,0,0] neg_hi:[1,0,0]
	v_pk_mul_f32 v[32:33], v[32:33], s[12:13] op_sel_hi:[1,0]
	v_pk_fma_f32 v[136:137], v[40:41], s[14:15], v[16:17] op_sel_hi:[1,0,0]
	v_pk_fma_f32 v[28:29], v[28:29], v[38:39], 0.5 op_sel_hi:[1,1,0] neg_lo:[1,0,0] neg_hi:[1,0,0]
	v_pk_mul_f32 v[18:19], v[18:19], v[20:21]
	v_pk_mul_f32 v[20:21], v[22:23], v[24:25]
	v_pk_mul_f32 v[8:9], v[200:201], v[132:133]
	v_pk_fma_f32 v[136:137], v[40:41], v[136:137], s[16:17] op_sel_hi:[1,1,0]
	v_pk_mul_f32 v[22:23], v[26:27], v[28:29]
	v_pk_fma_f32 v[0:1], v[0:1], 0.5, v[18:19] op_sel_hi:[1,0,1]
	v_pk_fma_f32 v[2:3], v[2:3], 0.5, v[20:21] op_sel_hi:[1,0,1]
	v_exp_f32_e32 v18, v32
	v_exp_f32_e32 v19, v33
	v_and_b32_e32 v21, 0x7fffffff, v9
	v_and_b32_e32 v20, 0x7fffffff, v8
	v_pk_fma_f32 v[136:137], v[40:41], v[136:137], s[8:9] op_sel_hi:[1,1,0]
	v_pk_fma_f32 v[4:5], v[4:5], 0.5, v[22:23] op_sel_hi:[1,0,1]
	v_pk_fma_f32 v[22:23], v[20:21], s[18:19], 1.0 op_sel_hi:[1,0,0]
	v_pk_fma_f32 v[136:137], v[40:41], v[136:137], s[10:11] op_sel_hi:[1,1,0]
	v_rcp_f32_e32 v22, v22
	v_rcp_f32_e32 v23, v23
	v_pk_mul_f32 v[40:41], v[40:41], v[136:137]
	v_pk_mul_f32 v[10:11], v[202:203], v[134:135]
	v_pk_fma_f32 v[18:19], v[18:19], v[40:41], 0.5 op_sel_hi:[1,1,0] neg_lo:[1,0,0] neg_hi:[1,0,0]
	v_and_b32_e32 v25, 0x7fffffff, v11
	v_pk_mul_f32 v[18:19], v[30:31], v[18:19]
	v_and_b32_e32 v24, 0x7fffffff, v10
	v_pk_fma_f32 v[6:7], v[6:7], 0.5, v[18:19] op_sel_hi:[1,0,1]
	v_pk_fma_f32 v[18:19], v[22:23], s[14:15], v[16:17] op_sel_hi:[1,0,0]
	v_pk_fma_f32 v[26:27], v[24:25], s[18:19], 1.0 op_sel_hi:[1,0,0]
	v_pk_fma_f32 v[18:19], v[22:23], v[18:19], s[16:17] op_sel_hi:[1,1,0]
	v_rcp_f32_e32 v26, v26
	v_pk_fma_f32 v[18:19], v[22:23], v[18:19], s[8:9] op_sel_hi:[1,1,0]
	v_rcp_f32_e32 v27, v27
	v_pk_fma_f32 v[18:19], v[22:23], v[18:19], s[10:11] op_sel_hi:[1,1,0]
	v_pk_mul_f32 v[12:13], v[204:205], v[128:129]
	v_pk_mul_f32 v[18:19], v[22:23], v[18:19]
	v_pk_mul_f32 v[22:23], v[8:9], v[8:9]
	v_pk_mul_f32 v[14:15], v[206:207], v[130:131]
	v_pk_mul_f32 v[22:23], v[22:23], s[12:13] op_sel_hi:[1,0]
	v_mov_b32_e32 v132, 0xffffff7f
	v_exp_f32_e32 v22, v22
	v_exp_f32_e32 v23, v23
	v_mov_b32_e32 v133, 0x64
	v_mov_b32_e32 v131, 0
	v_pk_fma_f32 v[18:19], v[22:23], v[18:19], 0.5 op_sel_hi:[1,1,0] neg_lo:[1,0,0] neg_hi:[1,0,0]
	s_nop 0
	v_pk_mul_f32 v[18:19], v[20:21], v[18:19]
	v_pk_mul_f32 v[20:21], v[10:11], v[10:11]
	v_pk_fma_f32 v[8:9], v[8:9], 0.5, v[18:19] op_sel_hi:[1,0,1]
	v_pk_fma_f32 v[18:19], v[26:27], s[14:15], v[16:17] op_sel_hi:[1,0,0]
	v_pk_mul_f32 v[20:21], v[20:21], s[12:13] op_sel_hi:[1,0]
	v_pk_fma_f32 v[18:19], v[26:27], v[18:19], s[16:17] op_sel_hi:[1,1,0]
	v_exp_f32_e32 v20, v20
	v_pk_fma_f32 v[18:19], v[26:27], v[18:19], s[8:9] op_sel_hi:[1,1,0]
	v_exp_f32_e32 v21, v21
	v_pk_fma_f32 v[18:19], v[26:27], v[18:19], s[10:11] op_sel_hi:[1,1,0]
	v_and_b32_e32 v23, 0x7fffffff, v13
	v_and_b32_e32 v22, 0x7fffffff, v12
	v_pk_mul_f32 v[18:19], v[26:27], v[18:19]
	v_pk_fma_f32 v[26:27], v[22:23], s[18:19], 1.0 op_sel_hi:[1,0,0]
	v_pk_fma_f32 v[18:19], v[20:21], v[18:19], 0.5 op_sel_hi:[1,1,0] neg_lo:[1,0,0] neg_hi:[1,0,0]
	v_rcp_f32_e32 v26, v26
	v_rcp_f32_e32 v27, v27
	v_pk_mul_f32 v[18:19], v[24:25], v[18:19]
	v_pk_mul_f32 v[20:21], v[12:13], v[12:13]
	v_pk_fma_f32 v[10:11], v[10:11], 0.5, v[18:19] op_sel_hi:[1,0,1]
	v_pk_fma_f32 v[18:19], v[26:27], s[14:15], v[16:17] op_sel_hi:[1,0,0]
	v_pk_mul_f32 v[20:21], v[20:21], s[12:13] op_sel_hi:[1,0]
	v_pk_fma_f32 v[18:19], v[26:27], v[18:19], s[16:17] op_sel_hi:[1,1,0]
	v_exp_f32_e32 v20, v20
	v_pk_fma_f32 v[18:19], v[26:27], v[18:19], s[8:9] op_sel_hi:[1,1,0]
	v_exp_f32_e32 v21, v21
	v_pk_fma_f32 v[18:19], v[26:27], v[18:19], s[10:11] op_sel_hi:[1,1,0]
	v_and_b32_e32 v25, 0x7fffffff, v15
	v_and_b32_e32 v24, 0x7fffffff, v14
	v_pk_mul_f32 v[18:19], v[26:27], v[18:19]
	v_pk_fma_f32 v[26:27], v[24:25], s[18:19], 1.0 op_sel_hi:[1,0,0]
	v_pk_fma_f32 v[18:19], v[20:21], v[18:19], 0.5 op_sel_hi:[1,1,0] neg_lo:[1,0,0] neg_hi:[1,0,0]
	v_rcp_f32_e32 v26, v26
	v_rcp_f32_e32 v27, v27
	v_pk_mul_f32 v[18:19], v[22:23], v[18:19]
	v_pk_fma_f32 v[16:17], v[26:27], s[14:15], v[16:17] op_sel_hi:[1,0,0]
	v_pk_fma_f32 v[12:13], v[12:13], 0.5, v[18:19] op_sel_hi:[1,0,1]
	v_pk_mul_f32 v[18:19], v[14:15], v[14:15]
	v_pk_fma_f32 v[16:17], v[26:27], v[16:17], s[16:17] op_sel_hi:[1,1,0]
	v_pk_mul_f32 v[18:19], v[18:19], s[12:13] op_sel_hi:[1,0]
	v_pk_fma_f32 v[16:17], v[26:27], v[16:17], s[8:9] op_sel_hi:[1,1,0]
	v_exp_f32_e32 v18, v18
	v_exp_f32_e32 v19, v19
	v_pk_fma_f32 v[16:17], v[26:27], v[16:17], s[10:11] op_sel_hi:[1,1,0]
	s_mov_b32 s9, 0x700000
	v_pk_mul_f32 v[16:17], v[26:27], v[16:17]
	s_nop 0
	v_pk_fma_f32 v[16:17], v[18:19], v[16:17], 0.5 op_sel_hi:[1,1,0] neg_lo:[1,0,0] neg_hi:[1,0,0]
	v_pk_mul_f32 v[16:17], v[24:25], v[16:17]
	s_nop 0
	v_pk_fma_f32 v[14:15], v[14:15], 0.5, v[16:17] op_sel_hi:[1,0,1]
	v_max3_f32 v16, |v6|, |v7|, |v0|
	v_max3_f32 v16, v16, |v1|, |v2|
	v_max3_f32 v16, v16, |v3|, |v4|
	v_max3_f32 v16, v16, |v5|, |v8|
	v_max3_f32 v16, v16, |v9|, |v10|
	v_max3_f32 v16, v16, |v11|, |v12|
	v_max3_f32 v16, v16, |v13|, |v14|
	v_max_f32_e64 v16, v16, |v15|
	v_mov_b32_e32 v17, v16
	s_nop 1
	v_permlane16_swap_b32_e32 v16, v17
	v_max_f32_e32 v16, v16, v17
	v_lshrrev_b32_e32 v17, 23, v16
	v_and_b32_e32 v16, 0x7fffff, v16
	v_cmp_lt_u32_e32 vcc, s9, v16
	s_nop 1
	v_addc_co_u32_e32 v16, vcc, v17, v132, vcc
	v_med3_i32 v129, v16, s13, v133
	v_lshlrev_b32_e32 v16, 23, v129
	v_sub_u32_e32 v16, 1.0, v16
	v_pk_mul_f32 v[40:41], v[16:17], v[8:9] op_sel_hi:[0,1]
	v_pk_mul_f32 v[42:43], v[16:17], v[10:11] op_sel_hi:[0,1]
	v_pk_mul_f32 v[44:45], v[16:17], v[12:13] op_sel_hi:[0,1]
	v_pk_mul_f32 v[46:47], v[16:17], v[14:15] op_sel_hi:[0,1]
	v_pk_mul_f32 v[32:33], v[16:17], v[0:1] op_sel_hi:[0,1]
	v_pk_mul_f32 v[34:35], v[16:17], v[2:3] op_sel_hi:[0,1]
	v_pk_mul_f32 v[36:37], v[16:17], v[4:5] op_sel_hi:[0,1]
	v_pk_mul_f32 v[38:39], v[16:17], v[6:7] op_sel_hi:[0,1]
	v_cvt_scalef32_2xpk16_fp6_f32 v[134:139], v[32:47], v[40:55], 1.0
	v_cvt_scalef32_pk32_f32_fp6 v[0:31], v[134:139], s15
	v_fma_f32 v16, v32, s20, v0
	v_fma_f32 v17, v33, s20, v2
	v_fma_f32 v18, v34, s20, v4
	v_fma_f32 v19, v35, s20, v6
	v_fma_f32 v20, v36, s20, v8
	v_fma_f32 v21, v37, s20, v10
	v_fma_f32 v22, v38, s20, v12
	v_fma_f32 v23, v39, s20, v14
	v_fma_f32 v24, v40, s20, v1
	v_fma_f32 v25, v41, s20, v3
	v_fma_f32 v26, v42, s20, v5
	v_fma_f32 v27, v43, s20, v7
	v_fma_f32 v28, v44, s20, v9
	v_fma_f32 v29, v45, s20, v11
	v_fma_f32 v30, v46, s20, v13
	v_fma_f32 v31, v47, s20, v15
	v_cvt_scalef32_2xpk16_fp6_f32 v[0:5], v[16:31], v[24:39], 1.0
	v_or_b32_e32 v3, 32, v181
	v_or_b32_e32 v4, v3, v180
	v_mul_u32_u24_e32 v130, 24, v4
	v_lshl_add_u64 v[4:5], v[168:169], 0, v[130:131]
	v_lshl_add_u64 v[4:5], v[4:5], 0, v[160:161]
	global_store_dwordx3 v[4:5], v[134:136], off nt
	v_add_co_u32_e32 v4, vcc, 0x1000, v4
	v_xor_b32_e32 v0, 0x20820820, v0
	v_xor_b32_e32 v1, 0x8208208, v1
	v_xor_b32_e32 v2, 0x82082082, v2
	v_addc_co_u32_e32 v5, vcc, 0, v5, vcc
	v_lshl_or_b32 v128, v3, 1, v180
	global_store_dwordx3 v[4:5], v[0:2], off offset:2048 nt
	s_and_saveexec_b64 s[24:25], s[0:1]
	s_cbranch_execz .LBB3_12
	v_mov_b32_e32 v1, 0x7a00
	v_add_u32_e32 v0, 0x7f, v129
	v_lshl_add_u32 v1, v129, 8, v1
	v_mov_b32_e32 v129, v131
	v_or_b32_e32 v2, v1, v0
	v_lshl_add_u64 v[0:1], v[166:167], 0, v[128:129]
	global_store_short v[0:1], v2, off
.LBB3_12:
	s_or_b64 exec, exec, s[24:25]
	v_permlane32_swap_b32_e32 v124, v116
	v_permlane32_swap_b32_e32 v125, v117
	v_permlane32_swap_b32_e32 v126, v118
	v_permlane32_swap_b32_e32 v127, v119
	v_permlane32_swap_b32_e32 v122, v114
	v_permlane32_swap_b32_e32 v123, v115
	v_permlane32_swap_b32_e32 v120, v112
	v_permlane32_swap_b32_e32 v121, v113
	v_mov_b64_e32 v[16:17], s[22:23]
	v_pk_mul_f32 v[0:1], v[192:193], v[124:125]
	v_pk_mul_f32 v[2:3], v[194:195], v[126:127]
	v_and_b32_e32 v19, 0x7fffffff, v1
	v_and_b32_e32 v18, 0x7fffffff, v0
	v_pk_mul_f32 v[6:7], v[198:199], v[122:123]
	v_and_b32_e32 v23, 0x7fffffff, v3
	v_and_b32_e32 v22, 0x7fffffff, v2
	v_pk_fma_f32 v[36:37], v[18:19], s[18:19], 1.0 op_sel_hi:[1,0,0]
	v_pk_mul_f32 v[4:5], v[196:197], v[120:121]
	v_and_b32_e32 v31, 0x7fffffff, v7
	v_and_b32_e32 v30, 0x7fffffff, v6
	v_pk_fma_f32 v[38:39], v[22:23], s[18:19], 1.0 op_sel_hi:[1,0,0]
	v_rcp_f32_e32 v36, v36
	v_rcp_f32_e32 v37, v37
	v_and_b32_e32 v27, 0x7fffffff, v5
	v_and_b32_e32 v26, 0x7fffffff, v4
	v_pk_fma_f32 v[42:43], v[30:31], s[18:19], 1.0 op_sel_hi:[1,0,0]
	v_rcp_f32_e32 v38, v38
	v_rcp_f32_e32 v39, v39
	v_pk_fma_f32 v[40:41], v[26:27], s[18:19], 1.0 op_sel_hi:[1,0,0]
	v_rcp_f32_e32 v42, v42
	v_rcp_f32_e32 v43, v43
	v_pk_mul_f32 v[20:21], v[0:1], v[0:1]
	v_rcp_f32_e32 v40, v40
	v_rcp_f32_e32 v41, v41
	v_pk_mul_f32 v[24:25], v[2:3], v[2:3]
	v_pk_mul_f32 v[20:21], v[20:21], s[12:13] op_sel_hi:[1,0]
	v_pk_fma_f32 v[46:47], v[36:37], s[14:15], v[16:17] op_sel_hi:[1,0,0]
	v_pk_mul_f32 v[8:9], v[200:201], v[116:117]
	v_pk_mul_f32 v[32:33], v[6:7], v[6:7]
	v_pk_mul_f32 v[24:25], v[24:25], s[12:13] op_sel_hi:[1,0]
	v_exp_f32_e32 v20, v20
	v_exp_f32_e32 v21, v21
	v_pk_fma_f32 v[116:117], v[38:39], s[14:15], v[16:17] op_sel_hi:[1,0,0]
	v_pk_fma_f32 v[46:47], v[36:37], v[46:47], s[16:17] op_sel_hi:[1,1,0]
	v_pk_mul_f32 v[28:29], v[4:5], v[4:5]
	v_pk_mul_f32 v[32:33], v[32:33], s[12:13] op_sel_hi:[1,0]
	v_exp_f32_e32 v24, v24
	v_exp_f32_e32 v25, v25
	v_pk_fma_f32 v[122:123], v[42:43], s[14:15], v[16:17] op_sel_hi:[1,0,0]
	v_pk_fma_f32 v[116:117], v[38:39], v[116:117], s[16:17] op_sel_hi:[1,1,0]
	v_pk_fma_f32 v[46:47], v[36:37], v[46:47], s[8:9] op_sel_hi:[1,1,0]
	v_and_b32_e32 v35, 0x7fffffff, v9
	v_and_b32_e32 v34, 0x7fffffff, v8
	v_pk_mul_f32 v[28:29], v[28:29], s[12:13] op_sel_hi:[1,0]
	v_exp_f32_e32 v32, v32
	v_exp_f32_e32 v33, v33
	v_pk_fma_f32 v[120:121], v[40:41], s[14:15], v[16:17] op_sel_hi:[1,0,0]
	v_pk_fma_f32 v[122:123], v[42:43], v[122:123], s[16:17] op_sel_hi:[1,1,0]
	v_pk_fma_f32 v[116:117], v[38:39], v[116:117], s[8:9] op_sel_hi:[1,1,0]
	v_pk_fma_f32 v[46:47], v[36:37], v[46:47], s[10:11] op_sel_hi:[1,1,0]
	v_pk_fma_f32 v[44:45], v[34:35], s[18:19], 1.0 op_sel_hi:[1,0,0]
	v_exp_f32_e32 v28, v28
	v_exp_f32_e32 v29, v29
	v_pk_fma_f32 v[120:121], v[40:41], v[120:121], s[16:17] op_sel_hi:[1,1,0]
	v_pk_fma_f32 v[122:123], v[42:43], v[122:123], s[8:9] op_sel_hi:[1,1,0]
	v_pk_fma_f32 v[116:117], v[38:39], v[116:117], s[10:11] op_sel_hi:[1,1,0]
	v_pk_mul_f32 v[36:37], v[36:37], v[46:47]
	v_rcp_f32_e32 v44, v44
	v_pk_fma_f32 v[120:121], v[40:41], v[120:121], s[8:9] op_sel_hi:[1,1,0]
	v_pk_fma_f32 v[122:123], v[42:43], v[122:123], s[10:11] op_sel_hi:[1,1,0]
	v_pk_mul_f32 v[38:39], v[38:39], v[116:117]
	v_pk_fma_f32 v[20:21], v[20:21], v[36:37], 0.5 op_sel_hi:[1,1,0] neg_lo:[1,0,0] neg_hi:[1,0,0]
	v_rcp_f32_e32 v45, v45
	v_pk_fma_f32 v[120:121], v[40:41], v[120:121], s[10:11] op_sel_hi:[1,1,0]
	v_pk_mul_f32 v[42:43], v[42:43], v[122:123]
	v_pk_fma_f32 v[24:25], v[24:25], v[38:39], 0.5 op_sel_hi:[1,1,0] neg_lo:[1,0,0] neg_hi:[1,0,0]
	v_pk_mul_f32 v[18:19], v[18:19], v[20:21]
	v_pk_mul_f32 v[40:41], v[40:41], v[120:121]
	v_pk_mul_f32 v[20:21], v[22:23], v[24:25]
	v_pk_fma_f32 v[0:1], v[0:1], 0.5, v[18:19] op_sel_hi:[1,0,1]
	v_pk_fma_f32 v[18:19], v[32:33], v[42:43], 0.5 op_sel_hi:[1,1,0] neg_lo:[1,0,0] neg_hi:[1,0,0]
	v_pk_fma_f32 v[28:29], v[28:29], v[40:41], 0.5 op_sel_hi:[1,1,0] neg_lo:[1,0,0] neg_hi:[1,0,0]
	v_pk_fma_f32 v[2:3], v[2:3], 0.5, v[20:21] op_sel_hi:[1,0,1]
	v_pk_mul_f32 v[18:19], v[30:31], v[18:19]
	v_pk_mul_f32 v[20:21], v[8:9], v[8:9]
	v_pk_mul_f32 v[22:23], v[26:27], v[28:29]
	v_pk_fma_f32 v[6:7], v[6:7], 0.5, v[18:19] op_sel_hi:[1,0,1]
	v_pk_fma_f32 v[18:19], v[44:45], s[14:15], v[16:17] op_sel_hi:[1,0,0]
	v_pk_mul_f32 v[20:21], v[20:21], s[12:13] op_sel_hi:[1,0]
	v_pk_mul_f32 v[10:11], v[202:203], v[118:119]
	v_pk_fma_f32 v[4:5], v[4:5], 0.5, v[22:23] op_sel_hi:[1,0,1]
	v_pk_fma_f32 v[18:19], v[44:45], v[18:19], s[16:17] op_sel_hi:[1,1,0]
	v_exp_f32_e32 v20, v20
	v_exp_f32_e32 v21, v21
	v_and_b32_e32 v23, 0x7fffffff, v11
	v_and_b32_e32 v22, 0x7fffffff, v10
	v_pk_fma_f32 v[18:19], v[44:45], v[18:19], s[8:9] op_sel_hi:[1,1,0]
	v_pk_fma_f32 v[24:25], v[22:23], s[18:19], 1.0 op_sel_hi:[1,0,0]
	v_pk_fma_f32 v[18:19], v[44:45], v[18:19], s[10:11] op_sel_hi:[1,1,0]
	v_rcp_f32_e32 v24, v24
	v_rcp_f32_e32 v25, v25
	v_pk_mul_f32 v[18:19], v[44:45], v[18:19]
	v_pk_mul_f32 v[12:13], v[204:205], v[112:113]
	v_pk_fma_f32 v[18:19], v[20:21], v[18:19], 0.5 op_sel_hi:[1,1,0] neg_lo:[1,0,0] neg_hi:[1,0,0]
	v_pk_mul_f32 v[20:21], v[10:11], v[10:11]
	v_pk_mul_f32 v[18:19], v[34:35], v[18:19]
	v_pk_mul_f32 v[20:21], v[20:21], s[12:13] op_sel_hi:[1,0]
	v_pk_fma_f32 v[8:9], v[8:9], 0.5, v[18:19] op_sel_hi:[1,0,1]
	v_pk_fma_f32 v[18:19], v[24:25], s[14:15], v[16:17] op_sel_hi:[1,0,0]
	v_exp_f32_e32 v20, v20
	v_pk_fma_f32 v[18:19], v[24:25], v[18:19], s[16:17] op_sel_hi:[1,1,0]
	v_exp_f32_e32 v21, v21
	v_pk_fma_f32 v[18:19], v[24:25], v[18:19], s[8:9] op_sel_hi:[1,1,0]
	v_pk_mul_f32 v[14:15], v[206:207], v[114:115]
	v_pk_fma_f32 v[18:19], v[24:25], v[18:19], s[10:11] op_sel_hi:[1,1,0]
	v_mov_b32_e32 v115, v131
	v_pk_mul_f32 v[18:19], v[24:25], v[18:19]
	v_and_b32_e32 v25, 0x7fffffff, v13
	v_and_b32_e32 v24, 0x7fffffff, v12
	v_pk_fma_f32 v[26:27], v[24:25], s[18:19], 1.0 op_sel_hi:[1,0,0]
	v_pk_fma_f32 v[18:19], v[20:21], v[18:19], 0.5 op_sel_hi:[1,1,0] neg_lo:[1,0,0] neg_hi:[1,0,0]
	v_rcp_f32_e32 v26, v26
	v_rcp_f32_e32 v27, v27
	v_pk_mul_f32 v[18:19], v[22:23], v[18:19]
	v_pk_mul_f32 v[20:21], v[12:13], v[12:13]
	v_pk_fma_f32 v[10:11], v[10:11], 0.5, v[18:19] op_sel_hi:[1,0,1]
	v_pk_fma_f32 v[18:19], v[26:27], s[14:15], v[16:17] op_sel_hi:[1,0,0]
	v_pk_mul_f32 v[20:21], v[20:21], s[12:13] op_sel_hi:[1,0]
	v_pk_fma_f32 v[18:19], v[26:27], v[18:19], s[16:17] op_sel_hi:[1,1,0]
	v_exp_f32_e32 v20, v20
	v_pk_fma_f32 v[18:19], v[26:27], v[18:19], s[8:9] op_sel_hi:[1,1,0]
	v_exp_f32_e32 v21, v21
	v_pk_fma_f32 v[18:19], v[26:27], v[18:19], s[10:11] op_sel_hi:[1,1,0]
	v_and_b32_e32 v23, 0x7fffffff, v15
	v_and_b32_e32 v22, 0x7fffffff, v14
	v_pk_mul_f32 v[18:19], v[26:27], v[18:19]
	v_pk_fma_f32 v[26:27], v[22:23], s[18:19], 1.0 op_sel_hi:[1,0,0]
	v_pk_fma_f32 v[18:19], v[20:21], v[18:19], 0.5 op_sel_hi:[1,1,0] neg_lo:[1,0,0] neg_hi:[1,0,0]
	v_rcp_f32_e32 v26, v26
	v_rcp_f32_e32 v27, v27
	v_pk_mul_f32 v[18:19], v[24:25], v[18:19]
	v_pk_fma_f32 v[16:17], v[26:27], s[14:15], v[16:17] op_sel_hi:[1,0,0]
	v_pk_fma_f32 v[12:13], v[12:13], 0.5, v[18:19] op_sel_hi:[1,0,1]
	v_pk_mul_f32 v[18:19], v[14:15], v[14:15]
	v_pk_fma_f32 v[16:17], v[26:27], v[16:17], s[16:17] op_sel_hi:[1,1,0]
	v_pk_mul_f32 v[18:19], v[18:19], s[12:13] op_sel_hi:[1,0]
	v_pk_fma_f32 v[16:17], v[26:27], v[16:17], s[8:9] op_sel_hi:[1,1,0]
	v_exp_f32_e32 v18, v18
	v_exp_f32_e32 v19, v19
	v_pk_fma_f32 v[16:17], v[26:27], v[16:17], s[10:11] op_sel_hi:[1,1,0]
	s_nop 0
	v_pk_mul_f32 v[16:17], v[26:27], v[16:17]
	s_nop 0
	v_pk_fma_f32 v[16:17], v[18:19], v[16:17], 0.5 op_sel_hi:[1,1,0] neg_lo:[1,0,0] neg_hi:[1,0,0]
	v_pk_mul_f32 v[16:17], v[22:23], v[16:17]
	s_nop 0
	v_pk_fma_f32 v[14:15], v[14:15], 0.5, v[16:17] op_sel_hi:[1,0,1]
	v_max3_f32 v16, |v6|, |v7|, |v0|
	v_max3_f32 v16, v16, |v1|, |v2|
	v_max3_f32 v16, v16, |v3|, |v4|
	v_max3_f32 v16, v16, |v5|, |v8|
	v_max3_f32 v16, v16, |v9|, |v10|
	v_max3_f32 v16, v16, |v11|, |v12|
	v_max3_f32 v16, v16, |v13|, |v14|
	v_max_f32_e64 v16, v16, |v15|
	v_mov_b32_e32 v17, v16
	s_nop 1
	v_permlane16_swap_b32_e32 v16, v17
	v_max_f32_e32 v16, v16, v17
	v_lshrrev_b32_e32 v17, 23, v16
	v_and_b32_e32 v16, 0x7fffff, v16
	v_cmp_lt_u32_e32 vcc, s9, v16
	s_nop 1
	v_addc_co_u32_e32 v16, vcc, v17, v132, vcc
	v_med3_i32 v113, v16, s13, v133
	v_lshlrev_b32_e32 v16, 23, v113
	v_sub_u32_e32 v16, 1.0, v16
	v_pk_mul_f32 v[40:41], v[16:17], v[8:9] op_sel_hi:[0,1]
	v_pk_mul_f32 v[42:43], v[16:17], v[10:11] op_sel_hi:[0,1]
	v_pk_mul_f32 v[44:45], v[16:17], v[12:13] op_sel_hi:[0,1]
	v_pk_mul_f32 v[46:47], v[16:17], v[14:15] op_sel_hi:[0,1]
	v_pk_mul_f32 v[32:33], v[16:17], v[0:1] op_sel_hi:[0,1]
	v_pk_mul_f32 v[34:35], v[16:17], v[2:3] op_sel_hi:[0,1]
	v_pk_mul_f32 v[36:37], v[16:17], v[4:5] op_sel_hi:[0,1]
	v_pk_mul_f32 v[38:39], v[16:17], v[6:7] op_sel_hi:[0,1]
	v_cvt_scalef32_2xpk16_fp6_f32 v[116:121], v[32:47], v[40:55], 1.0
	v_cvt_scalef32_pk32_f32_fp6 v[0:31], v[116:121], s15
	v_fma_f32 v16, v32, s20, v0
	v_fma_f32 v17, v33, s20, v2
	v_fma_f32 v18, v34, s20, v4
	v_fma_f32 v19, v35, s20, v6
	v_fma_f32 v20, v36, s20, v8
	v_fma_f32 v21, v37, s20, v10
	v_fma_f32 v22, v38, s20, v12
	v_fma_f32 v23, v39, s20, v14
	v_fma_f32 v24, v40, s20, v1
	v_fma_f32 v25, v41, s20, v3
	v_fma_f32 v26, v42, s20, v5
	v_fma_f32 v27, v43, s20, v7
	v_fma_f32 v28, v44, s20, v9
	v_fma_f32 v29, v45, s20, v11
	v_fma_f32 v30, v46, s20, v13
	v_fma_f32 v31, v47, s20, v15
	v_cvt_scalef32_2xpk16_fp6_f32 v[0:5], v[16:31], v[24:39], 1.0
	v_or_b32_e32 v3, 48, v181
	v_or_b32_e32 v4, v3, v180
	v_mul_u32_u24_e32 v114, 24, v4
	v_lshl_add_u64 v[4:5], v[168:169], 0, v[114:115]
	v_lshl_add_u64 v[4:5], v[4:5], 0, v[160:161]
	global_store_dwordx3 v[4:5], v[116:118], off nt
	v_add_co_u32_e32 v4, vcc, 0x1000, v4
	v_xor_b32_e32 v0, 0x20820820, v0
	v_xor_b32_e32 v1, 0x8208208, v1
	v_xor_b32_e32 v2, 0x82082082, v2
	v_addc_co_u32_e32 v5, vcc, 0, v5, vcc
	v_lshl_or_b32 v112, v3, 1, v180
	global_store_dwordx3 v[4:5], v[0:2], off offset:2048 nt
	s_and_saveexec_b64 s[8:9], s[0:1]
	s_cbranch_execz .LBB3_14
	v_mov_b32_e32 v1, 0x7a00
	v_add_u32_e32 v0, 0x7f, v113
	v_lshl_add_u32 v1, v113, 8, v1
	v_mov_b32_e32 v113, 0
	v_or_b32_e32 v2, v1, v0
	v_lshl_add_u64 v[0:1], v[166:167], 0, v[112:113]
	global_store_short v[0:1], v2, off
.LBB3_14:
	s_or_b64 exec, exec, s[8:9]
	v_or_b32_e32 v8, 2, v178
	v_or_b32_e32 v0, v8, v177
	v_lshlrev_b32_e32 v20, 5, v0
	v_or_b32_e32 v12, v20, v179
	v_ashrrev_i32_e32 v13, 31, v12
	v_lshl_add_u64 v[120:121], v[12:13], 2, s[4:5]
	v_ashrrev_i32_e32 v13, 31, v20
	v_lshl_add_u64 v[122:123], v[12:13], 2, s[4:5]
	v_ashrrev_i32_e32 v12, 1, v8
	v_add_u32_e32 v18, s11, v12
	s_movk_i32 s9, 0x6000
	v_mov_b64_e32 v[14:15], s[2:3]
	v_ashrrev_i32_e32 v19, 31, v18
	v_or_b32_e32 v12, v20, v176
	v_mad_i64_i32 v[118:119], s[20:21], v18, s9, v[14:15]
	v_lshlrev_b64 v[14:15], 10, v[18:19]
	v_lshl_add_u64 v[124:125], v[12:13], 2, s[4:5]
	v_lshl_add_u64 v[116:117], s[6:7], 0, v[14:15]
	v_permlane32_swap_b32_e32 v108, v100
	v_permlane32_swap_b32_e32 v109, v101
	s_mov_b32 s16, 0x3e6d3388
	v_permlane32_swap_b32_e32 v110, v102
	v_permlane32_swap_b32_e32 v111, v103
	v_permlane32_swap_b32_e32 v104, v96
	v_permlane32_swap_b32_e32 v105, v97
	s_mov_b32 s18, 0xbf3a00e3
	s_mov_b32 s12, 0x3f07dc22
	s_mov_b32 s10, 0xbf38aa3b
	v_mov_b64_e32 v[16:17], s[18:19]
	s_mov_b32 s14, 0x3f35f0e3
	s_mov_b32 s2, 0xbe11a98e
	s_mov_b32 s8, 0x3e027906
	v_permlane32_swap_b32_e32 v106, v98
	v_permlane32_swap_b32_e32 v107, v99
	s_movk_i32 s5, 0xff9c
	s_mov_b32 s4, 0xc2000000
	s_waitcnt vmcnt(8)
	v_pk_mul_f32 v[0:1], v[208:209], v[108:109]
	s_nop 0
	v_and_b32_e32 v19, 0x7fffffff, v1
	v_and_b32_e32 v18, 0x7fffffff, v0
	v_pk_fma_f32 v[26:27], v[18:19], s[16:17], 1.0 op_sel_hi:[1,0,0]
	v_pk_mul_f32 v[2:3], v[210:211], v[110:111]
	v_rcp_f32_e32 v26, v26
	v_rcp_f32_e32 v27, v27
	v_and_b32_e32 v23, 0x7fffffff, v3
	v_and_b32_e32 v22, 0x7fffffff, v2
	v_pk_mul_f32 v[4:5], v[212:213], v[104:105]
	v_pk_fma_f32 v[28:29], v[22:23], s[16:17], 1.0 op_sel_hi:[1,0,0]
	v_pk_mul_f32 v[20:21], v[0:1], v[0:1]
	v_and_b32_e32 v31, 0x7fffffff, v5
	v_and_b32_e32 v30, 0x7fffffff, v4
	v_rcp_f32_e32 v28, v28
	v_rcp_f32_e32 v29, v29
	v_pk_mul_f32 v[20:21], v[20:21], s[10:11] op_sel_hi:[1,0]
	v_pk_fma_f32 v[36:37], v[30:31], s[16:17], 1.0 op_sel_hi:[1,0,0]
	v_pk_fma_f32 v[38:39], v[26:27], s[12:13], v[16:17] op_sel_hi:[1,0,0]
	v_exp_f32_e32 v20, v20
	v_exp_f32_e32 v21, v21
	v_rcp_f32_e32 v36, v36
	v_rcp_f32_e32 v37, v37
	v_pk_fma_f32 v[38:39], v[26:27], v[38:39], s[14:15] op_sel_hi:[1,1,0]
	v_pk_mul_f32 v[24:25], v[2:3], v[2:3]
	v_pk_fma_f32 v[38:39], v[26:27], v[38:39], s[2:3] op_sel_hi:[1,1,0]
	v_pk_mul_f32 v[24:25], v[24:25], s[10:11] op_sel_hi:[1,0]
	v_pk_fma_f32 v[40:41], v[28:29], s[12:13], v[16:17] op_sel_hi:[1,0,0]
	v_pk_fma_f32 v[38:39], v[26:27], v[38:39], s[8:9] op_sel_hi:[1,1,0]
	v_pk_mul_f32 v[32:33], v[4:5], v[4:5]
	v_exp_f32_e32 v24, v24
	v_exp_f32_e32 v25, v25
	v_pk_fma_f32 v[40:41], v[28:29], v[40:41], s[14:15] op_sel_hi:[1,1,0]
	v_pk_mul_f32 v[26:27], v[26:27], v[38:39]
	v_pk_mul_f32 v[6:7], v[214:215], v[106:107]
	v_pk_mul_f32 v[32:33], v[32:33], s[10:11] op_sel_hi:[1,0]
	v_pk_fma_f32 v[42:43], v[36:37], s[12:13], v[16:17] op_sel_hi:[1,0,0]
	v_pk_fma_f32 v[40:41], v[28:29], v[40:41], s[2:3] op_sel_hi:[1,1,0]
	v_pk_fma_f32 v[20:21], v[20:21], v[26:27], 0.5 op_sel_hi:[1,1,0] neg_lo:[1,0,0] neg_hi:[1,0,0]
	v_and_b32_e32 v35, 0x7fffffff, v7
	v_and_b32_e32 v34, 0x7fffffff, v6
	v_exp_f32_e32 v32, v32
	v_exp_f32_e32 v33, v33
	v_pk_fma_f32 v[42:43], v[36:37], v[42:43], s[14:15] op_sel_hi:[1,1,0]
	v_pk_fma_f32 v[40:41], v[28:29], v[40:41], s[8:9] op_sel_hi:[1,1,0]
	v_pk_mul_f32 v[18:19], v[18:19], v[20:21]
	v_pk_fma_f32 v[42:43], v[36:37], v[42:43], s[2:3] op_sel_hi:[1,1,0]
	v_pk_mul_f32 v[28:29], v[28:29], v[40:41]
	v_pk_fma_f32 v[0:1], v[0:1], 0.5, v[18:19] op_sel_hi:[1,0,1]
	v_pk_fma_f32 v[18:19], v[34:35], s[16:17], 1.0 op_sel_hi:[1,0,0]
	v_pk_fma_f32 v[38:39], v[36:37], v[42:43], s[8:9] op_sel_hi:[1,1,0]
	v_pk_fma_f32 v[24:25], v[24:25], v[28:29], 0.5 op_sel_hi:[1,1,0] neg_lo:[1,0,0] neg_hi:[1,0,0]
	v_rcp_f32_e32 v18, v18
	v_rcp_f32_e32 v19, v19
	v_pk_mul_f32 v[26:27], v[36:37], v[38:39]
	v_pk_mul_f32 v[20:21], v[22:23], v[24:25]
	v_pk_mul_f32 v[8:9], v[216:217], v[100:101]
	v_pk_fma_f32 v[2:3], v[2:3], 0.5, v[20:21] op_sel_hi:[1,0,1]
	v_pk_fma_f32 v[20:21], v[32:33], v[26:27], 0.5 op_sel_hi:[1,1,0] neg_lo:[1,0,0] neg_hi:[1,0,0]
	v_and_b32_e32 v23, 0x7fffffff, v9
	v_pk_mul_f32 v[20:21], v[30:31], v[20:21]
	v_and_b32_e32 v22, 0x7fffffff, v8
	v_pk_fma_f32 v[4:5], v[4:5], 0.5, v[20:21] op_sel_hi:[1,0,1]
	v_pk_fma_f32 v[20:21], v[18:19], s[12:13], v[16:17] op_sel_hi:[1,0,0]
	v_pk_fma_f32 v[24:25], v[22:23], s[16:17], 1.0 op_sel_hi:[1,0,0]
	v_pk_fma_f32 v[20:21], v[18:19], v[20:21], s[14:15] op_sel_hi:[1,1,0]
	v_rcp_f32_e32 v24, v24
	v_pk_fma_f32 v[20:21], v[18:19], v[20:21], s[2:3] op_sel_hi:[1,1,0]
	v_rcp_f32_e32 v25, v25
	v_pk_fma_f32 v[20:21], v[18:19], v[20:21], s[8:9] op_sel_hi:[1,1,0]
	v_pk_mul_f32 v[10:11], v[218:219], v[102:103]
	v_pk_mul_f32 v[18:19], v[18:19], v[20:21]
	v_pk_mul_f32 v[20:21], v[6:7], v[6:7]
	v_pk_mul_f32 v[12:13], v[220:221], v[96:97]
	v_pk_mul_f32 v[20:21], v[20:21], s[10:11] op_sel_hi:[1,0]
	v_pk_mul_f32 v[14:15], v[222:223], v[98:99]
	v_exp_f32_e32 v20, v20
	v_exp_f32_e32 v21, v21
	v_mov_b32_e32 v96, 0xffffff7f
	v_mov_b32_e32 v97, 0x64
	v_pk_fma_f32 v[18:19], v[20:21], v[18:19], 0.5 op_sel_hi:[1,1,0] neg_lo:[1,0,0] neg_hi:[1,0,0]
	s_nop 0
	v_pk_mul_f32 v[18:19], v[34:35], v[18:19]
	v_pk_mul_f32 v[20:21], v[8:9], v[8:9]
	v_pk_fma_f32 v[6:7], v[6:7], 0.5, v[18:19] op_sel_hi:[1,0,1]
	v_pk_fma_f32 v[18:19], v[24:25], s[12:13], v[16:17] op_sel_hi:[1,0,0]
	v_pk_mul_f32 v[20:21], v[20:21], s[10:11] op_sel_hi:[1,0]
	v_pk_fma_f32 v[18:19], v[24:25], v[18:19], s[14:15] op_sel_hi:[1,1,0]
	v_exp_f32_e32 v20, v20
	v_pk_fma_f32 v[18:19], v[24:25], v[18:19], s[2:3] op_sel_hi:[1,1,0]
	v_exp_f32_e32 v21, v21
	v_pk_fma_f32 v[18:19], v[24:25], v[18:19], s[8:9] op_sel_hi:[1,1,0]
	s_nop 0
	v_pk_mul_f32 v[18:19], v[24:25], v[18:19]
	v_and_b32_e32 v25, 0x7fffffff, v11
	v_and_b32_e32 v24, 0x7fffffff, v10
	v_pk_fma_f32 v[26:27], v[24:25], s[16:17], 1.0 op_sel_hi:[1,0,0]
	v_pk_fma_f32 v[18:19], v[20:21], v[18:19], 0.5 op_sel_hi:[1,1,0] neg_lo:[1,0,0] neg_hi:[1,0,0]
	v_rcp_f32_e32 v26, v26
	v_rcp_f32_e32 v27, v27
	v_pk_mul_f32 v[18:19], v[22:23], v[18:19]
	v_pk_mul_f32 v[20:21], v[10:11], v[10:11]
	v_pk_fma_f32 v[8:9], v[8:9], 0.5, v[18:19] op_sel_hi:[1,0,1]
	v_pk_fma_f32 v[18:19], v[26:27], s[12:13], v[16:17] op_sel_hi:[1,0,0]
	v_pk_mul_f32 v[20:21], v[20:21], s[10:11] op_sel_hi:[1,0]
	v_pk_fma_f32 v[18:19], v[26:27], v[18:19], s[14:15] op_sel_hi:[1,1,0]
	v_exp_f32_e32 v20, v20
	v_pk_fma_f32 v[18:19], v[26:27], v[18:19], s[2:3] op_sel_hi:[1,1,0]
	v_exp_f32_e32 v21, v21
	v_pk_fma_f32 v[18:19], v[26:27], v[18:19], s[8:9] op_sel_hi:[1,1,0]
	v_and_b32_e32 v23, 0x7fffffff, v13
	v_and_b32_e32 v22, 0x7fffffff, v12
	v_pk_mul_f32 v[18:19], v[26:27], v[18:19]
	v_pk_fma_f32 v[26:27], v[22:23], s[16:17], 1.0 op_sel_hi:[1,0,0]
	v_pk_fma_f32 v[18:19], v[20:21], v[18:19], 0.5 op_sel_hi:[1,1,0] neg_lo:[1,0,0] neg_hi:[1,0,0]
	v_rcp_f32_e32 v26, v26
	v_rcp_f32_e32 v27, v27
	v_pk_mul_f32 v[18:19], v[24:25], v[18:19]
	v_pk_mul_f32 v[20:21], v[12:13], v[12:13]
	v_pk_fma_f32 v[10:11], v[10:11], 0.5, v[18:19] op_sel_hi:[1,0,1]
	v_pk_fma_f32 v[18:19], v[26:27], s[12:13], v[16:17] op_sel_hi:[1,0,0]
	v_pk_mul_f32 v[20:21], v[20:21], s[10:11] op_sel_hi:[1,0]
	v_pk_fma_f32 v[18:19], v[26:27], v[18:19], s[14:15] op_sel_hi:[1,1,0]
	v_exp_f32_e32 v20, v20
	v_pk_fma_f32 v[18:19], v[26:27], v[18:19], s[2:3] op_sel_hi:[1,1,0]
	v_exp_f32_e32 v21, v21
	v_pk_fma_f32 v[18:19], v[26:27], v[18:19], s[8:9] op_sel_hi:[1,1,0]
	v_and_b32_e32 v25, 0x7fffffff, v15
	v_and_b32_e32 v24, 0x7fffffff, v14
	v_pk_mul_f32 v[18:19], v[26:27], v[18:19]
	v_pk_fma_f32 v[26:27], v[24:25], s[16:17], 1.0 op_sel_hi:[1,0,0]
	v_pk_fma_f32 v[18:19], v[20:21], v[18:19], 0.5 op_sel_hi:[1,1,0] neg_lo:[1,0,0] neg_hi:[1,0,0]
	v_rcp_f32_e32 v26, v26
	v_rcp_f32_e32 v27, v27
	v_pk_mul_f32 v[18:19], v[22:23], v[18:19]
	v_pk_fma_f32 v[16:17], v[26:27], s[12:13], v[16:17] op_sel_hi:[1,0,0]
	v_pk_fma_f32 v[12:13], v[12:13], 0.5, v[18:19] op_sel_hi:[1,0,1]
	v_pk_mul_f32 v[18:19], v[14:15], v[14:15]
	v_pk_fma_f32 v[16:17], v[26:27], v[16:17], s[14:15] op_sel_hi:[1,1,0]
	v_pk_mul_f32 v[18:19], v[18:19], s[10:11] op_sel_hi:[1,0]
	v_pk_fma_f32 v[16:17], v[26:27], v[16:17], s[2:3] op_sel_hi:[1,1,0]
	v_exp_f32_e32 v18, v18
	v_exp_f32_e32 v19, v19
	v_pk_fma_f32 v[16:17], v[26:27], v[16:17], s[8:9] op_sel_hi:[1,1,0]
	s_mov_b32 s3, 0x700000
	v_pk_mul_f32 v[16:17], v[26:27], v[16:17]
	s_mov_b32 s9, 0x42000000
	v_pk_fma_f32 v[16:17], v[18:19], v[16:17], 0.5 op_sel_hi:[1,1,0] neg_lo:[1,0,0] neg_hi:[1,0,0]
	v_pk_mul_f32 v[16:17], v[24:25], v[16:17]
	s_nop 0
	v_pk_fma_f32 v[14:15], v[14:15], 0.5, v[16:17] op_sel_hi:[1,0,1]
	v_max3_f32 v16, |v6|, |v7|, |v0|
	v_max3_f32 v16, v16, |v1|, |v2|
	v_max3_f32 v16, v16, |v3|, |v4|
	v_max3_f32 v16, v16, |v5|, |v8|
	v_max3_f32 v16, v16, |v9|, |v10|
	v_max3_f32 v16, v16, |v11|, |v12|
	v_max3_f32 v16, v16, |v13|, |v14|
	v_max_f32_e64 v16, v16, |v15|
	v_mov_b32_e32 v17, v16
	s_nop 1
	v_permlane16_swap_b32_e32 v16, v17
	v_max_f32_e32 v16, v16, v17
	v_lshrrev_b32_e32 v17, 23, v16
	v_and_b32_e32 v16, 0x7fffff, v16
	v_cmp_lt_u32_e32 vcc, s3, v16
	s_nop 1
	v_addc_co_u32_e32 v16, vcc, v17, v96, vcc
	v_med3_i32 v98, v16, s5, v97
	v_lshlrev_b32_e32 v16, 23, v98
	v_sub_u32_e32 v16, 1.0, v16
	v_pk_mul_f32 v[40:41], v[16:17], v[8:9] op_sel_hi:[0,1]
	v_pk_mul_f32 v[42:43], v[16:17], v[10:11] op_sel_hi:[0,1]
	v_pk_mul_f32 v[44:45], v[16:17], v[12:13] op_sel_hi:[0,1]
	v_pk_mul_f32 v[46:47], v[16:17], v[14:15] op_sel_hi:[0,1]
	v_pk_mul_f32 v[32:33], v[16:17], v[0:1] op_sel_hi:[0,1]
	v_pk_mul_f32 v[34:35], v[16:17], v[2:3] op_sel_hi:[0,1]
	v_pk_mul_f32 v[36:37], v[16:17], v[4:5] op_sel_hi:[0,1]
	v_pk_mul_f32 v[38:39], v[16:17], v[6:7] op_sel_hi:[0,1]
	v_cvt_scalef32_2xpk16_fp6_f32 v[100:105], v[32:47], v[40:55], 1.0
	v_cvt_scalef32_pk32_f32_fp6 v[0:31], v[100:105], s9
	v_fma_f32 v16, v32, s4, v0
	v_fma_f32 v17, v33, s4, v2
	v_fma_f32 v18, v34, s4, v4
	v_fma_f32 v19, v35, s4, v6
	v_fma_f32 v20, v36, s4, v8
	v_fma_f32 v21, v37, s4, v10
	v_fma_f32 v22, v38, s4, v12
	v_fma_f32 v23, v39, s4, v14
	v_fma_f32 v24, v40, s4, v1
	v_fma_f32 v25, v41, s4, v3
	v_fma_f32 v26, v42, s4, v5
	v_fma_f32 v27, v43, s4, v7
	v_fma_f32 v28, v44, s4, v9
	v_fma_f32 v29, v45, s4, v11
	v_fma_f32 v30, v46, s4, v13
	v_fma_f32 v31, v47, s4, v15
	v_cvt_scalef32_2xpk16_fp6_f32 v[0:5], v[16:31], v[24:39], 1.0
	v_lshl_add_u64 v[4:5], v[118:119], 0, v[164:165]
	v_lshl_add_u64 v[4:5], v[4:5], 0, v[160:161]
	global_store_dwordx3 v[4:5], v[100:102], off nt
	v_add_co_u32_e32 v4, vcc, 0x1000, v4
	v_xor_b32_e32 v0, 0x20820820, v0
	v_xor_b32_e32 v1, 0x8208208, v1
	v_xor_b32_e32 v2, 0x82082082, v2
	v_addc_co_u32_e32 v5, vcc, 0, v5, vcc
	global_store_dwordx3 v[4:5], v[0:2], off offset:2048 nt
	s_and_saveexec_b64 s[6:7], s[0:1]
	s_cbranch_execz .LBB3_16
	v_mov_b32_e32 v1, 0x7a00
	v_add_u32_e32 v0, 0x7f, v98
	v_lshl_add_u32 v1, v98, 8, v1
	v_mov_b32_e32 v163, 0
	v_or_b32_e32 v2, v1, v0
	v_lshl_add_u64 v[0:1], v[116:117], 0, v[162:163]
	global_store_short v[0:1], v2, off
.LBB3_16:
	s_or_b64 exec, exec, s[6:7]
	v_permlane32_swap_b32_e32 v92, v84
	v_permlane32_swap_b32_e32 v93, v85
	v_permlane32_swap_b32_e32 v94, v86
	v_permlane32_swap_b32_e32 v95, v87
	v_permlane32_swap_b32_e32 v90, v82
	v_permlane32_swap_b32_e32 v91, v83
	v_permlane32_swap_b32_e32 v88, v80
	v_permlane32_swap_b32_e32 v89, v81
	v_mov_b64_e32 v[16:17], s[18:19]
	v_pk_mul_f32 v[0:1], v[208:209], v[92:93]
	v_pk_mul_f32 v[2:3], v[210:211], v[94:95]
	v_and_b32_e32 v19, 0x7fffffff, v1
	v_and_b32_e32 v18, 0x7fffffff, v0
	v_pk_mul_f32 v[6:7], v[214:215], v[90:91]
	v_and_b32_e32 v23, 0x7fffffff, v3
	v_and_b32_e32 v22, 0x7fffffff, v2
	v_pk_fma_f32 v[36:37], v[18:19], s[16:17], 1.0 op_sel_hi:[1,0,0]
	v_pk_mul_f32 v[4:5], v[212:213], v[88:89]
	v_and_b32_e32 v31, 0x7fffffff, v7
	v_and_b32_e32 v30, 0x7fffffff, v6
	v_pk_fma_f32 v[38:39], v[22:23], s[16:17], 1.0 op_sel_hi:[1,0,0]
	v_rcp_f32_e32 v36, v36
	v_rcp_f32_e32 v37, v37
	v_and_b32_e32 v27, 0x7fffffff, v5
	v_and_b32_e32 v26, 0x7fffffff, v4
	v_pk_fma_f32 v[42:43], v[30:31], s[16:17], 1.0 op_sel_hi:[1,0,0]
	v_rcp_f32_e32 v38, v38
	v_rcp_f32_e32 v39, v39
	v_pk_fma_f32 v[40:41], v[26:27], s[16:17], 1.0 op_sel_hi:[1,0,0]
	v_rcp_f32_e32 v42, v42
	v_rcp_f32_e32 v43, v43
	v_pk_mul_f32 v[20:21], v[0:1], v[0:1]
	v_rcp_f32_e32 v40, v40
	v_rcp_f32_e32 v41, v41
	v_pk_mul_f32 v[24:25], v[2:3], v[2:3]
	v_pk_mul_f32 v[20:21], v[20:21], s[10:11] op_sel_hi:[1,0]
	v_pk_fma_f32 v[46:47], v[36:37], s[12:13], v[16:17] op_sel_hi:[1,0,0]
	v_pk_mul_f32 v[8:9], v[216:217], v[84:85]
	v_pk_mul_f32 v[32:33], v[6:7], v[6:7]
	v_pk_mul_f32 v[24:25], v[24:25], s[10:11] op_sel_hi:[1,0]
	v_exp_f32_e32 v20, v20
	v_exp_f32_e32 v21, v21
	v_pk_fma_f32 v[84:85], v[38:39], s[12:13], v[16:17] op_sel_hi:[1,0,0]
	v_pk_fma_f32 v[46:47], v[36:37], v[46:47], s[14:15] op_sel_hi:[1,1,0]
	v_pk_mul_f32 v[28:29], v[4:5], v[4:5]
	v_pk_mul_f32 v[32:33], v[32:33], s[10:11] op_sel_hi:[1,0]
	v_exp_f32_e32 v24, v24
	v_exp_f32_e32 v25, v25
	v_pk_fma_f32 v[90:91], v[42:43], s[12:13], v[16:17] op_sel_hi:[1,0,0]
	v_pk_fma_f32 v[84:85], v[38:39], v[84:85], s[14:15] op_sel_hi:[1,1,0]
	v_pk_fma_f32 v[46:47], v[36:37], v[46:47], s[2:3] op_sel_hi:[1,1,0]
	v_and_b32_e32 v35, 0x7fffffff, v9
	v_and_b32_e32 v34, 0x7fffffff, v8
	v_pk_mul_f32 v[28:29], v[28:29], s[10:11] op_sel_hi:[1,0]
	v_exp_f32_e32 v32, v32
	v_exp_f32_e32 v33, v33
	v_pk_fma_f32 v[88:89], v[40:41], s[12:13], v[16:17] op_sel_hi:[1,0,0]
	v_pk_fma_f32 v[90:91], v[42:43], v[90:91], s[14:15] op_sel_hi:[1,1,0]
	v_pk_fma_f32 v[84:85], v[38:39], v[84:85], s[2:3] op_sel_hi:[1,1,0]
	v_pk_fma_f32 v[46:47], v[36:37], v[46:47], s[8:9] op_sel_hi:[1,1,0]
	v_pk_fma_f32 v[44:45], v[34:35], s[16:17], 1.0 op_sel_hi:[1,0,0]
	v_exp_f32_e32 v28, v28
	v_exp_f32_e32 v29, v29
	v_pk_fma_f32 v[88:89], v[40:41], v[88:89], s[14:15] op_sel_hi:[1,1,0]
	v_pk_fma_f32 v[90:91], v[42:43], v[90:91], s[2:3] op_sel_hi:[1,1,0]
	v_pk_fma_f32 v[84:85], v[38:39], v[84:85], s[8:9] op_sel_hi:[1,1,0]
	v_pk_mul_f32 v[36:37], v[36:37], v[46:47]
	v_rcp_f32_e32 v44, v44
	v_pk_fma_f32 v[88:89], v[40:41], v[88:89], s[2:3] op_sel_hi:[1,1,0]
	v_pk_fma_f32 v[90:91], v[42:43], v[90:91], s[8:9] op_sel_hi:[1,1,0]
	v_pk_mul_f32 v[38:39], v[38:39], v[84:85]
	v_pk_fma_f32 v[20:21], v[20:21], v[36:37], 0.5 op_sel_hi:[1,1,0] neg_lo:[1,0,0] neg_hi:[1,0,0]
	v_rcp_f32_e32 v45, v45
	v_pk_fma_f32 v[88:89], v[40:41], v[88:89], s[8:9] op_sel_hi:[1,1,0]
	v_pk_mul_f32 v[42:43], v[42:43], v[90:91]
	v_pk_fma_f32 v[24:25], v[24:25], v[38:39], 0.5 op_sel_hi:[1,1,0] neg_lo:[1,0,0] neg_hi:[1,0,0]
	v_pk_mul_f32 v[18:19], v[18:19], v[20:21]
	v_pk_mul_f32 v[40:41], v[40:41], v[88:89]
	v_pk_mul_f32 v[20:21], v[22:23], v[24:25]
	v_pk_fma_f32 v[0:1], v[0:1], 0.5, v[18:19] op_sel_hi:[1,0,1]
	v_pk_fma_f32 v[18:19], v[32:33], v[42:43], 0.5 op_sel_hi:[1,1,0] neg_lo:[1,0,0] neg_hi:[1,0,0]
	v_pk_fma_f32 v[28:29], v[28:29], v[40:41], 0.5 op_sel_hi:[1,1,0] neg_lo:[1,0,0] neg_hi:[1,0,0]
	v_pk_fma_f32 v[2:3], v[2:3], 0.5, v[20:21] op_sel_hi:[1,0,1]
	v_pk_mul_f32 v[18:19], v[30:31], v[18:19]
	v_pk_mul_f32 v[20:21], v[8:9], v[8:9]
	v_pk_mul_f32 v[22:23], v[26:27], v[28:29]
	v_pk_fma_f32 v[6:7], v[6:7], 0.5, v[18:19] op_sel_hi:[1,0,1]
	v_pk_fma_f32 v[18:19], v[44:45], s[12:13], v[16:17] op_sel_hi:[1,0,0]
	v_pk_mul_f32 v[20:21], v[20:21], s[10:11] op_sel_hi:[1,0]
	v_pk_mul_f32 v[10:11], v[218:219], v[86:87]
	v_pk_fma_f32 v[4:5], v[4:5], 0.5, v[22:23] op_sel_hi:[1,0,1]
	v_pk_fma_f32 v[18:19], v[44:45], v[18:19], s[14:15] op_sel_hi:[1,1,0]
	v_exp_f32_e32 v20, v20
	v_exp_f32_e32 v21, v21
	v_and_b32_e32 v23, 0x7fffffff, v11
	v_and_b32_e32 v22, 0x7fffffff, v10
	v_pk_fma_f32 v[18:19], v[44:45], v[18:19], s[2:3] op_sel_hi:[1,1,0]
	v_pk_fma_f32 v[24:25], v[22:23], s[16:17], 1.0 op_sel_hi:[1,0,0]
	v_pk_fma_f32 v[18:19], v[44:45], v[18:19], s[8:9] op_sel_hi:[1,1,0]
	v_rcp_f32_e32 v24, v24
	v_rcp_f32_e32 v25, v25
	v_pk_mul_f32 v[18:19], v[44:45], v[18:19]
	v_pk_mul_f32 v[12:13], v[220:221], v[80:81]
	v_pk_fma_f32 v[18:19], v[20:21], v[18:19], 0.5 op_sel_hi:[1,1,0] neg_lo:[1,0,0] neg_hi:[1,0,0]
	v_pk_mul_f32 v[20:21], v[10:11], v[10:11]
	v_pk_mul_f32 v[18:19], v[34:35], v[18:19]
	v_pk_mul_f32 v[20:21], v[20:21], s[10:11] op_sel_hi:[1,0]
	v_pk_fma_f32 v[8:9], v[8:9], 0.5, v[18:19] op_sel_hi:[1,0,1]
	v_pk_fma_f32 v[18:19], v[24:25], s[12:13], v[16:17] op_sel_hi:[1,0,0]
	v_exp_f32_e32 v20, v20
	v_pk_fma_f32 v[18:19], v[24:25], v[18:19], s[14:15] op_sel_hi:[1,1,0]
	v_exp_f32_e32 v21, v21
	v_pk_fma_f32 v[18:19], v[24:25], v[18:19], s[2:3] op_sel_hi:[1,1,0]
	v_pk_mul_f32 v[14:15], v[222:223], v[82:83]
	v_pk_fma_f32 v[18:19], v[24:25], v[18:19], s[8:9] op_sel_hi:[1,1,0]
	s_nop 0
	v_pk_mul_f32 v[18:19], v[24:25], v[18:19]
	v_and_b32_e32 v25, 0x7fffffff, v13
	v_and_b32_e32 v24, 0x7fffffff, v12
	v_pk_fma_f32 v[26:27], v[24:25], s[16:17], 1.0 op_sel_hi:[1,0,0]
	v_pk_fma_f32 v[18:19], v[20:21], v[18:19], 0.5 op_sel_hi:[1,1,0] neg_lo:[1,0,0] neg_hi:[1,0,0]
	v_rcp_f32_e32 v26, v26
	v_rcp_f32_e32 v27, v27
	v_pk_mul_f32 v[18:19], v[22:23], v[18:19]
	v_pk_mul_f32 v[20:21], v[12:13], v[12:13]
	v_pk_fma_f32 v[10:11], v[10:11], 0.5, v[18:19] op_sel_hi:[1,0,1]
	v_pk_fma_f32 v[18:19], v[26:27], s[12:13], v[16:17] op_sel_hi:[1,0,0]
	v_pk_mul_f32 v[20:21], v[20:21], s[10:11] op_sel_hi:[1,0]
	v_pk_fma_f32 v[18:19], v[26:27], v[18:19], s[14:15] op_sel_hi:[1,1,0]
	v_exp_f32_e32 v20, v20
	v_pk_fma_f32 v[18:19], v[26:27], v[18:19], s[2:3] op_sel_hi:[1,1,0]
	v_exp_f32_e32 v21, v21
	v_pk_fma_f32 v[18:19], v[26:27], v[18:19], s[8:9] op_sel_hi:[1,1,0]
	v_and_b32_e32 v23, 0x7fffffff, v15
	v_and_b32_e32 v22, 0x7fffffff, v14
	v_pk_mul_f32 v[18:19], v[26:27], v[18:19]
	v_pk_fma_f32 v[26:27], v[22:23], s[16:17], 1.0 op_sel_hi:[1,0,0]
	v_pk_fma_f32 v[18:19], v[20:21], v[18:19], 0.5 op_sel_hi:[1,1,0] neg_lo:[1,0,0] neg_hi:[1,0,0]
	v_rcp_f32_e32 v26, v26
	v_rcp_f32_e32 v27, v27
	v_pk_mul_f32 v[18:19], v[24:25], v[18:19]
	v_pk_fma_f32 v[16:17], v[26:27], s[12:13], v[16:17] op_sel_hi:[1,0,0]
	v_pk_fma_f32 v[12:13], v[12:13], 0.5, v[18:19] op_sel_hi:[1,0,1]
	v_pk_mul_f32 v[18:19], v[14:15], v[14:15]
	v_pk_fma_f32 v[16:17], v[26:27], v[16:17], s[14:15] op_sel_hi:[1,1,0]
	v_pk_mul_f32 v[18:19], v[18:19], s[10:11] op_sel_hi:[1,0]
	v_pk_fma_f32 v[16:17], v[26:27], v[16:17], s[2:3] op_sel_hi:[1,1,0]
	v_exp_f32_e32 v18, v18
	v_exp_f32_e32 v19, v19
	v_pk_fma_f32 v[16:17], v[26:27], v[16:17], s[8:9] op_sel_hi:[1,1,0]
	s_nop 0
	v_pk_mul_f32 v[16:17], v[26:27], v[16:17]
	s_nop 0
	v_pk_fma_f32 v[16:17], v[18:19], v[16:17], 0.5 op_sel_hi:[1,1,0] neg_lo:[1,0,0] neg_hi:[1,0,0]
	v_pk_mul_f32 v[16:17], v[22:23], v[16:17]
	s_nop 0
	v_pk_fma_f32 v[14:15], v[14:15], 0.5, v[16:17] op_sel_hi:[1,0,1]
	v_max3_f32 v16, |v6|, |v7|, |v0|
	v_max3_f32 v16, v16, |v1|, |v2|
	v_max3_f32 v16, v16, |v3|, |v4|
	v_max3_f32 v16, v16, |v5|, |v8|
	v_max3_f32 v16, v16, |v9|, |v10|
	v_max3_f32 v16, v16, |v11|, |v12|
	v_max3_f32 v16, v16, |v13|, |v14|
	v_max_f32_e64 v16, v16, |v15|
	v_mov_b32_e32 v17, v16
	s_nop 1
	v_permlane16_swap_b32_e32 v16, v17
	v_max_f32_e32 v16, v16, v17
	v_lshrrev_b32_e32 v17, 23, v16
	v_and_b32_e32 v16, 0x7fffff, v16
	v_cmp_lt_u32_e32 vcc, s3, v16
	s_nop 1
	v_addc_co_u32_e32 v16, vcc, v17, v96, vcc
	v_med3_i32 v80, v16, s5, v97
	v_lshlrev_b32_e32 v16, 23, v80
	v_sub_u32_e32 v16, 1.0, v16
	v_pk_mul_f32 v[40:41], v[16:17], v[8:9] op_sel_hi:[0,1]
	v_pk_mul_f32 v[42:43], v[16:17], v[10:11] op_sel_hi:[0,1]
	v_pk_mul_f32 v[44:45], v[16:17], v[12:13] op_sel_hi:[0,1]
	v_pk_mul_f32 v[46:47], v[16:17], v[14:15] op_sel_hi:[0,1]
	v_pk_mul_f32 v[32:33], v[16:17], v[0:1] op_sel_hi:[0,1]
	v_pk_mul_f32 v[34:35], v[16:17], v[2:3] op_sel_hi:[0,1]
	v_pk_mul_f32 v[36:37], v[16:17], v[4:5] op_sel_hi:[0,1]
	v_pk_mul_f32 v[38:39], v[16:17], v[6:7] op_sel_hi:[0,1]
	v_cvt_scalef32_2xpk16_fp6_f32 v[82:87], v[32:47], v[40:55], 1.0
	v_cvt_scalef32_pk32_f32_fp6 v[0:31], v[82:87], s9
	v_fma_f32 v16, v32, s4, v0
	v_fma_f32 v17, v33, s4, v2
	v_fma_f32 v18, v34, s4, v4
	v_fma_f32 v19, v35, s4, v6
	v_fma_f32 v20, v36, s4, v8
	v_fma_f32 v21, v37, s4, v10
	v_fma_f32 v22, v38, s4, v12
	v_fma_f32 v23, v39, s4, v14
	v_fma_f32 v24, v40, s4, v1
	v_fma_f32 v25, v41, s4, v3
	v_fma_f32 v26, v42, s4, v5
	v_fma_f32 v27, v43, s4, v7
	v_fma_f32 v28, v44, s4, v9
	v_fma_f32 v29, v45, s4, v11
	v_fma_f32 v30, v46, s4, v13
	v_fma_f32 v31, v47, s4, v15
	v_cvt_scalef32_2xpk16_fp6_f32 v[0:5], v[16:31], v[24:39], 1.0
	v_lshl_add_u64 v[4:5], v[118:119], 0, v[146:147]
	v_lshl_add_u64 v[4:5], v[4:5], 0, v[160:161]
	global_store_dwordx3 v[4:5], v[82:84], off nt
	v_add_co_u32_e32 v4, vcc, 0x1000, v4
	v_xor_b32_e32 v0, 0x20820820, v0
	v_xor_b32_e32 v1, 0x8208208, v1
	v_xor_b32_e32 v2, 0x82082082, v2
	v_addc_co_u32_e32 v5, vcc, 0, v5, vcc
	global_store_dwordx3 v[4:5], v[0:2], off offset:2048 nt
	s_and_saveexec_b64 s[2:3], s[0:1]
	s_cbranch_execz .LBB3_18
	v_mov_b32_e32 v1, 0x7a00
	v_add_u32_e32 v0, 0x7f, v80
	v_lshl_add_u32 v1, v80, 8, v1
	v_mov_b32_e32 v145, 0
	v_or_b32_e32 v2, v1, v0
	v_lshl_add_u64 v[0:1], v[116:117], 0, v[144:145]
	global_store_short v[0:1], v2, off
.LBB3_18:
	s_or_b64 exec, exec, s[2:3]
	v_permlane32_swap_b32_e32 v76, v68
	v_permlane32_swap_b32_e32 v77, v69
	v_permlane32_swap_b32_e32 v78, v70
	v_permlane32_swap_b32_e32 v79, v71
	v_permlane32_swap_b32_e32 v72, v64
	v_permlane32_swap_b32_e32 v73, v65
	s_mov_b32 s12, 0x3e6d3388
	v_permlane32_swap_b32_e32 v74, v66
	v_permlane32_swap_b32_e32 v75, v67
	s_mov_b32 s16, 0xbf3a00e3
	s_mov_b32 s8, 0x3f07dc22
	s_mov_b32 s6, 0xbf38aa3b
	v_mov_b64_e32 v[16:17], s[16:17]
	s_mov_b32 s10, 0x3f35f0e3
	s_mov_b32 s2, 0xbe11a98e
	s_mov_b32 s4, 0x3e027906
	s_mov_b32 s14, 0xc2000000
	v_pk_mul_f32 v[0:1], v[208:209], v[76:77]
	v_pk_mul_f32 v[2:3], v[210:211], v[78:79]
	v_pk_mul_f32 v[4:5], v[212:213], v[72:73]
	v_and_b32_e32 v19, 0x7fffffff, v1
	v_and_b32_e32 v18, 0x7fffffff, v0
	v_and_b32_e32 v23, 0x7fffffff, v3
	v_and_b32_e32 v22, 0x7fffffff, v2
	v_and_b32_e32 v27, 0x7fffffff, v5
	v_and_b32_e32 v26, 0x7fffffff, v4
	v_pk_fma_f32 v[34:35], v[18:19], s[12:13], 1.0 op_sel_hi:[1,0,0]
	v_pk_fma_f32 v[36:37], v[22:23], s[12:13], 1.0 op_sel_hi:[1,0,0]
	v_pk_fma_f32 v[38:39], v[26:27], s[12:13], 1.0 op_sel_hi:[1,0,0]
	v_rcp_f32_e32 v34, v34
	v_rcp_f32_e32 v35, v35
	v_rcp_f32_e32 v36, v36
	v_rcp_f32_e32 v37, v37
	v_rcp_f32_e32 v38, v38
	v_rcp_f32_e32 v39, v39
	v_pk_mul_f32 v[6:7], v[214:215], v[74:75]
	v_pk_mul_f32 v[20:21], v[0:1], v[0:1]
	v_pk_mul_f32 v[24:25], v[2:3], v[2:3]
	v_pk_mul_f32 v[28:29], v[4:5], v[4:5]
	v_and_b32_e32 v31, 0x7fffffff, v7
	v_and_b32_e32 v30, 0x7fffffff, v6
	v_pk_mul_f32 v[20:21], v[20:21], s[6:7] op_sel_hi:[1,0]
	v_pk_mul_f32 v[24:25], v[24:25], s[6:7] op_sel_hi:[1,0]
	v_pk_fma_f32 v[42:43], v[34:35], s[8:9], v[16:17] op_sel_hi:[1,0,0]
	v_pk_fma_f32 v[44:45], v[36:37], s[8:9], v[16:17] op_sel_hi:[1,0,0]
	v_pk_mul_f32 v[28:29], v[28:29], s[6:7] op_sel_hi:[1,0]
	v_pk_fma_f32 v[40:41], v[30:31], s[12:13], 1.0 op_sel_hi:[1,0,0]
	v_exp_f32_e32 v20, v20
	v_exp_f32_e32 v21, v21
	v_exp_f32_e32 v24, v24
	v_exp_f32_e32 v25, v25
	v_pk_fma_f32 v[46:47], v[38:39], s[8:9], v[16:17] op_sel_hi:[1,0,0]
	v_pk_fma_f32 v[42:43], v[34:35], v[42:43], s[10:11] op_sel_hi:[1,1,0]
	v_pk_fma_f32 v[44:45], v[36:37], v[44:45], s[10:11] op_sel_hi:[1,1,0]
	v_exp_f32_e32 v28, v28
	v_exp_f32_e32 v29, v29
	v_rcp_f32_e32 v40, v40
	v_rcp_f32_e32 v41, v41
	v_pk_fma_f32 v[46:47], v[38:39], v[46:47], s[10:11] op_sel_hi:[1,1,0]
	v_pk_fma_f32 v[42:43], v[34:35], v[42:43], s[2:3] op_sel_hi:[1,1,0]
	v_pk_fma_f32 v[44:45], v[36:37], v[44:45], s[2:3] op_sel_hi:[1,1,0]
	v_pk_fma_f32 v[46:47], v[38:39], v[46:47], s[2:3] op_sel_hi:[1,1,0]
	v_pk_fma_f32 v[42:43], v[34:35], v[42:43], s[4:5] op_sel_hi:[1,1,0]
	v_pk_fma_f32 v[44:45], v[36:37], v[44:45], s[4:5] op_sel_hi:[1,1,0]
	v_pk_fma_f32 v[46:47], v[38:39], v[46:47], s[4:5] op_sel_hi:[1,1,0]
	v_pk_mul_f32 v[34:35], v[34:35], v[42:43]
	v_pk_mul_f32 v[36:37], v[36:37], v[44:45]
	v_pk_mul_f32 v[32:33], v[6:7], v[6:7]
	v_pk_mul_f32 v[38:39], v[38:39], v[46:47]
	v_pk_fma_f32 v[20:21], v[20:21], v[34:35], 0.5 op_sel_hi:[1,1,0] neg_lo:[1,0,0] neg_hi:[1,0,0]
	v_pk_fma_f32 v[24:25], v[24:25], v[36:37], 0.5 op_sel_hi:[1,1,0] neg_lo:[1,0,0] neg_hi:[1,0,0]
	v_pk_mul_f32 v[32:33], v[32:33], s[6:7] op_sel_hi:[1,0]
	v_pk_fma_f32 v[72:73], v[40:41], s[8:9], v[16:17] op_sel_hi:[1,0,0]
	v_pk_fma_f32 v[28:29], v[28:29], v[38:39], 0.5 op_sel_hi:[1,1,0] neg_lo:[1,0,0] neg_hi:[1,0,0]
	v_pk_mul_f32 v[18:19], v[18:19], v[20:21]
	v_pk_mul_f32 v[20:21], v[22:23], v[24:25]
	v_pk_mul_f32 v[8:9], v[216:217], v[68:69]
	v_pk_fma_f32 v[72:73], v[40:41], v[72:73], s[10:11] op_sel_hi:[1,1,0]
	v_pk_mul_f32 v[22:23], v[26:27], v[28:29]
	v_pk_fma_f32 v[0:1], v[0:1], 0.5, v[18:19] op_sel_hi:[1,0,1]
	v_pk_fma_f32 v[2:3], v[2:3], 0.5, v[20:21] op_sel_hi:[1,0,1]
	v_exp_f32_e32 v18, v32
	v_exp_f32_e32 v19, v33
	v_and_b32_e32 v21, 0x7fffffff, v9
	v_and_b32_e32 v20, 0x7fffffff, v8
	v_pk_fma_f32 v[72:73], v[40:41], v[72:73], s[2:3] op_sel_hi:[1,1,0]
	v_pk_fma_f32 v[4:5], v[4:5], 0.5, v[22:23] op_sel_hi:[1,0,1]
	v_pk_fma_f32 v[22:23], v[20:21], s[12:13], 1.0 op_sel_hi:[1,0,0]
	v_pk_fma_f32 v[72:73], v[40:41], v[72:73], s[4:5] op_sel_hi:[1,1,0]
	v_rcp_f32_e32 v22, v22
	v_rcp_f32_e32 v23, v23
	v_pk_mul_f32 v[40:41], v[40:41], v[72:73]
	v_pk_mul_f32 v[10:11], v[218:219], v[70:71]
	v_pk_fma_f32 v[18:19], v[18:19], v[40:41], 0.5 op_sel_hi:[1,1,0] neg_lo:[1,0,0] neg_hi:[1,0,0]
	v_and_b32_e32 v25, 0x7fffffff, v11
	v_pk_mul_f32 v[18:19], v[30:31], v[18:19]
	v_and_b32_e32 v24, 0x7fffffff, v10
	v_pk_fma_f32 v[6:7], v[6:7], 0.5, v[18:19] op_sel_hi:[1,0,1]
	v_pk_fma_f32 v[18:19], v[22:23], s[8:9], v[16:17] op_sel_hi:[1,0,0]
	v_pk_fma_f32 v[26:27], v[24:25], s[12:13], 1.0 op_sel_hi:[1,0,0]
	v_pk_fma_f32 v[18:19], v[22:23], v[18:19], s[10:11] op_sel_hi:[1,1,0]
	v_rcp_f32_e32 v26, v26
	v_pk_fma_f32 v[18:19], v[22:23], v[18:19], s[2:3] op_sel_hi:[1,1,0]
	v_rcp_f32_e32 v27, v27
	v_pk_fma_f32 v[18:19], v[22:23], v[18:19], s[4:5] op_sel_hi:[1,1,0]
	v_pk_mul_f32 v[12:13], v[220:221], v[64:65]
	v_pk_mul_f32 v[18:19], v[22:23], v[18:19]
	v_pk_mul_f32 v[22:23], v[8:9], v[8:9]
	v_pk_mul_f32 v[14:15], v[222:223], v[66:67]
	v_pk_mul_f32 v[22:23], v[22:23], s[6:7] op_sel_hi:[1,0]
	v_mov_b32_e32 v64, 0xffffff7f
	v_exp_f32_e32 v22, v22
	v_exp_f32_e32 v23, v23
	v_mov_b32_e32 v65, 0x64
	v_pk_fma_f32 v[18:19], v[22:23], v[18:19], 0.5 op_sel_hi:[1,1,0] neg_lo:[1,0,0] neg_hi:[1,0,0]
	s_nop 0
	v_pk_mul_f32 v[18:19], v[20:21], v[18:19]
	v_pk_mul_f32 v[20:21], v[10:11], v[10:11]
	v_pk_fma_f32 v[8:9], v[8:9], 0.5, v[18:19] op_sel_hi:[1,0,1]
	v_pk_fma_f32 v[18:19], v[26:27], s[8:9], v[16:17] op_sel_hi:[1,0,0]
	v_pk_mul_f32 v[20:21], v[20:21], s[6:7] op_sel_hi:[1,0]
	v_pk_fma_f32 v[18:19], v[26:27], v[18:19], s[10:11] op_sel_hi:[1,1,0]
	v_exp_f32_e32 v20, v20
	v_pk_fma_f32 v[18:19], v[26:27], v[18:19], s[2:3] op_sel_hi:[1,1,0]
	v_exp_f32_e32 v21, v21
	v_pk_fma_f32 v[18:19], v[26:27], v[18:19], s[4:5] op_sel_hi:[1,1,0]
	v_and_b32_e32 v23, 0x7fffffff, v13
	v_and_b32_e32 v22, 0x7fffffff, v12
	v_pk_mul_f32 v[18:19], v[26:27], v[18:19]
	v_pk_fma_f32 v[26:27], v[22:23], s[12:13], 1.0 op_sel_hi:[1,0,0]
	v_pk_fma_f32 v[18:19], v[20:21], v[18:19], 0.5 op_sel_hi:[1,1,0] neg_lo:[1,0,0] neg_hi:[1,0,0]
	v_rcp_f32_e32 v26, v26
	v_rcp_f32_e32 v27, v27
	v_pk_mul_f32 v[18:19], v[24:25], v[18:19]
	v_pk_mul_f32 v[20:21], v[12:13], v[12:13]
	v_pk_fma_f32 v[10:11], v[10:11], 0.5, v[18:19] op_sel_hi:[1,0,1]
	v_pk_fma_f32 v[18:19], v[26:27], s[8:9], v[16:17] op_sel_hi:[1,0,0]
	v_pk_mul_f32 v[20:21], v[20:21], s[6:7] op_sel_hi:[1,0]
	v_pk_fma_f32 v[18:19], v[26:27], v[18:19], s[10:11] op_sel_hi:[1,1,0]
	v_exp_f32_e32 v20, v20
	v_pk_fma_f32 v[18:19], v[26:27], v[18:19], s[2:3] op_sel_hi:[1,1,0]
	v_exp_f32_e32 v21, v21
	v_pk_fma_f32 v[18:19], v[26:27], v[18:19], s[4:5] op_sel_hi:[1,1,0]
	v_and_b32_e32 v25, 0x7fffffff, v15
	v_and_b32_e32 v24, 0x7fffffff, v14
	v_pk_mul_f32 v[18:19], v[26:27], v[18:19]
	v_pk_fma_f32 v[26:27], v[24:25], s[12:13], 1.0 op_sel_hi:[1,0,0]
	v_pk_fma_f32 v[18:19], v[20:21], v[18:19], 0.5 op_sel_hi:[1,1,0] neg_lo:[1,0,0] neg_hi:[1,0,0]
	v_rcp_f32_e32 v26, v26
	v_rcp_f32_e32 v27, v27
	v_pk_mul_f32 v[18:19], v[22:23], v[18:19]
	v_pk_fma_f32 v[16:17], v[26:27], s[8:9], v[16:17] op_sel_hi:[1,0,0]
	v_pk_fma_f32 v[12:13], v[12:13], 0.5, v[18:19] op_sel_hi:[1,0,1]
	v_pk_mul_f32 v[18:19], v[14:15], v[14:15]
	v_pk_fma_f32 v[16:17], v[26:27], v[16:17], s[10:11] op_sel_hi:[1,1,0]
	v_pk_mul_f32 v[18:19], v[18:19], s[6:7] op_sel_hi:[1,0]
	v_pk_fma_f32 v[16:17], v[26:27], v[16:17], s[2:3] op_sel_hi:[1,1,0]
	v_exp_f32_e32 v18, v18
	v_exp_f32_e32 v19, v19
	v_pk_fma_f32 v[16:17], v[26:27], v[16:17], s[4:5] op_sel_hi:[1,1,0]
	s_mov_b32 s3, 0x700000
	v_pk_mul_f32 v[16:17], v[26:27], v[16:17]
	s_mov_b32 s7, 0x42000000
	v_pk_fma_f32 v[16:17], v[18:19], v[16:17], 0.5 op_sel_hi:[1,1,0] neg_lo:[1,0,0] neg_hi:[1,0,0]
	v_pk_mul_f32 v[16:17], v[24:25], v[16:17]
	s_nop 0
	v_pk_fma_f32 v[14:15], v[14:15], 0.5, v[16:17] op_sel_hi:[1,0,1]
	v_max3_f32 v16, |v6|, |v7|, |v0|
	v_max3_f32 v16, v16, |v1|, |v2|
	v_max3_f32 v16, v16, |v3|, |v4|
	v_max3_f32 v16, v16, |v5|, |v8|
	v_max3_f32 v16, v16, |v9|, |v10|
	v_max3_f32 v16, v16, |v11|, |v12|
	v_max3_f32 v16, v16, |v13|, |v14|
	v_max_f32_e64 v16, v16, |v15|
	v_mov_b32_e32 v17, v16
	s_nop 1
	v_permlane16_swap_b32_e32 v16, v17
	v_max_f32_e32 v16, v16, v17
	v_lshrrev_b32_e32 v17, 23, v16
	v_and_b32_e32 v16, 0x7fffff, v16
	v_cmp_lt_u32_e32 vcc, s3, v16
	s_nop 1
	v_addc_co_u32_e32 v16, vcc, v17, v64, vcc
	v_med3_i32 v66, v16, s5, v65
	v_lshlrev_b32_e32 v16, 23, v66
	v_sub_u32_e32 v16, 1.0, v16
	v_pk_mul_f32 v[40:41], v[16:17], v[8:9] op_sel_hi:[0,1]
	v_pk_mul_f32 v[42:43], v[16:17], v[10:11] op_sel_hi:[0,1]
	v_pk_mul_f32 v[44:45], v[16:17], v[12:13] op_sel_hi:[0,1]
	v_pk_mul_f32 v[46:47], v[16:17], v[14:15] op_sel_hi:[0,1]
	v_pk_mul_f32 v[32:33], v[16:17], v[0:1] op_sel_hi:[0,1]
	v_pk_mul_f32 v[34:35], v[16:17], v[2:3] op_sel_hi:[0,1]
	v_pk_mul_f32 v[36:37], v[16:17], v[4:5] op_sel_hi:[0,1]
	v_pk_mul_f32 v[38:39], v[16:17], v[6:7] op_sel_hi:[0,1]
	v_cvt_scalef32_2xpk16_fp6_f32 v[68:73], v[32:47], v[40:55], 1.0
	v_cvt_scalef32_pk32_f32_fp6 v[0:31], v[68:73], s7
	v_fma_f32 v16, v32, s14, v0
	v_fma_f32 v17, v33, s14, v2
	v_fma_f32 v18, v34, s14, v4
	v_fma_f32 v19, v35, s14, v6
	v_fma_f32 v20, v36, s14, v8
	v_fma_f32 v21, v37, s14, v10
	v_fma_f32 v22, v38, s14, v12
	v_fma_f32 v23, v39, s14, v14
	v_fma_f32 v24, v40, s14, v1
	v_fma_f32 v25, v41, s14, v3
	v_fma_f32 v26, v42, s14, v5
	v_fma_f32 v27, v43, s14, v7
	v_fma_f32 v28, v44, s14, v9
	v_fma_f32 v29, v45, s14, v11
	v_fma_f32 v30, v46, s14, v13
	v_fma_f32 v31, v47, s14, v15
	v_cvt_scalef32_2xpk16_fp6_f32 v[0:5], v[16:31], v[24:39], 1.0
	v_lshl_add_u64 v[4:5], v[118:119], 0, v[130:131]
	v_lshl_add_u64 v[4:5], v[4:5], 0, v[160:161]
	global_store_dwordx3 v[4:5], v[68:70], off nt
	v_add_co_u32_e32 v4, vcc, 0x1000, v4
	v_xor_b32_e32 v0, 0x20820820, v0
	v_xor_b32_e32 v1, 0x8208208, v1
	v_xor_b32_e32 v2, 0x82082082, v2
	v_addc_co_u32_e32 v5, vcc, 0, v5, vcc
	global_store_dwordx3 v[4:5], v[0:2], off offset:2048 nt
	s_and_saveexec_b64 s[18:19], s[0:1]
	s_cbranch_execz .LBB3_20
	v_mov_b32_e32 v1, 0x7a00
	v_add_u32_e32 v0, 0x7f, v66
	v_lshl_add_u32 v1, v66, 8, v1
	v_mov_b32_e32 v129, 0
	v_or_b32_e32 v2, v1, v0
	v_lshl_add_u64 v[0:1], v[116:117], 0, v[128:129]
	global_store_short v[0:1], v2, off
.LBB3_20:
	s_or_b64 exec, exec, s[18:19]
	v_permlane32_swap_b32_e32 v60, v52
	v_permlane32_swap_b32_e32 v61, v53
	v_permlane32_swap_b32_e32 v62, v54
	v_permlane32_swap_b32_e32 v63, v55
	v_permlane32_swap_b32_e32 v58, v50
	v_permlane32_swap_b32_e32 v59, v51
	v_permlane32_swap_b32_e32 v56, v48
	v_permlane32_swap_b32_e32 v57, v49
	v_mov_b64_e32 v[16:17], s[16:17]
	v_pk_mul_f32 v[0:1], v[208:209], v[60:61]
	v_pk_mul_f32 v[2:3], v[210:211], v[62:63]
	v_and_b32_e32 v19, 0x7fffffff, v1
	v_and_b32_e32 v18, 0x7fffffff, v0
	v_pk_mul_f32 v[6:7], v[214:215], v[58:59]
	v_and_b32_e32 v23, 0x7fffffff, v3
	v_and_b32_e32 v22, 0x7fffffff, v2
	v_pk_fma_f32 v[36:37], v[18:19], s[12:13], 1.0 op_sel_hi:[1,0,0]
	v_pk_mul_f32 v[4:5], v[212:213], v[56:57]
	v_and_b32_e32 v31, 0x7fffffff, v7
	v_and_b32_e32 v30, 0x7fffffff, v6
	v_pk_fma_f32 v[38:39], v[22:23], s[12:13], 1.0 op_sel_hi:[1,0,0]
	v_rcp_f32_e32 v36, v36
	v_rcp_f32_e32 v37, v37
	v_and_b32_e32 v27, 0x7fffffff, v5
	v_and_b32_e32 v26, 0x7fffffff, v4
	v_pk_fma_f32 v[42:43], v[30:31], s[12:13], 1.0 op_sel_hi:[1,0,0]
	v_rcp_f32_e32 v38, v38
	v_rcp_f32_e32 v39, v39
	v_pk_fma_f32 v[40:41], v[26:27], s[12:13], 1.0 op_sel_hi:[1,0,0]
	v_rcp_f32_e32 v42, v42
	v_rcp_f32_e32 v43, v43
	v_pk_mul_f32 v[20:21], v[0:1], v[0:1]
	v_rcp_f32_e32 v40, v40
	v_rcp_f32_e32 v41, v41
	v_pk_mul_f32 v[24:25], v[2:3], v[2:3]
	v_pk_mul_f32 v[20:21], v[20:21], s[6:7] op_sel_hi:[1,0]
	v_pk_fma_f32 v[46:47], v[36:37], s[8:9], v[16:17] op_sel_hi:[1,0,0]
	v_pk_mul_f32 v[8:9], v[216:217], v[52:53]
	v_pk_mul_f32 v[32:33], v[6:7], v[6:7]
	v_pk_mul_f32 v[24:25], v[24:25], s[6:7] op_sel_hi:[1,0]
	v_exp_f32_e32 v20, v20
	v_exp_f32_e32 v21, v21
	v_pk_fma_f32 v[52:53], v[38:39], s[8:9], v[16:17] op_sel_hi:[1,0,0]
	v_pk_fma_f32 v[46:47], v[36:37], v[46:47], s[10:11] op_sel_hi:[1,1,0]
	v_pk_mul_f32 v[28:29], v[4:5], v[4:5]
	v_pk_mul_f32 v[32:33], v[32:33], s[6:7] op_sel_hi:[1,0]
	v_exp_f32_e32 v24, v24
	v_exp_f32_e32 v25, v25
	v_pk_fma_f32 v[58:59], v[42:43], s[8:9], v[16:17] op_sel_hi:[1,0,0]
	v_pk_fma_f32 v[52:53], v[38:39], v[52:53], s[10:11] op_sel_hi:[1,1,0]
	v_pk_fma_f32 v[46:47], v[36:37], v[46:47], s[2:3] op_sel_hi:[1,1,0]
	v_and_b32_e32 v35, 0x7fffffff, v9
	v_and_b32_e32 v34, 0x7fffffff, v8
	v_pk_mul_f32 v[28:29], v[28:29], s[6:7] op_sel_hi:[1,0]
	v_exp_f32_e32 v32, v32
	v_exp_f32_e32 v33, v33
	v_pk_fma_f32 v[56:57], v[40:41], s[8:9], v[16:17] op_sel_hi:[1,0,0]
	v_pk_fma_f32 v[58:59], v[42:43], v[58:59], s[10:11] op_sel_hi:[1,1,0]
	v_pk_fma_f32 v[52:53], v[38:39], v[52:53], s[2:3] op_sel_hi:[1,1,0]
	v_pk_fma_f32 v[46:47], v[36:37], v[46:47], s[4:5] op_sel_hi:[1,1,0]
	v_pk_fma_f32 v[44:45], v[34:35], s[12:13], 1.0 op_sel_hi:[1,0,0]
	v_exp_f32_e32 v28, v28
	v_exp_f32_e32 v29, v29
	v_pk_fma_f32 v[56:57], v[40:41], v[56:57], s[10:11] op_sel_hi:[1,1,0]
	v_pk_fma_f32 v[58:59], v[42:43], v[58:59], s[2:3] op_sel_hi:[1,1,0]
	v_pk_fma_f32 v[52:53], v[38:39], v[52:53], s[4:5] op_sel_hi:[1,1,0]
	v_pk_mul_f32 v[36:37], v[36:37], v[46:47]
	v_rcp_f32_e32 v44, v44
	v_pk_fma_f32 v[56:57], v[40:41], v[56:57], s[2:3] op_sel_hi:[1,1,0]
	v_pk_fma_f32 v[58:59], v[42:43], v[58:59], s[4:5] op_sel_hi:[1,1,0]
	v_pk_mul_f32 v[38:39], v[38:39], v[52:53]
	v_pk_fma_f32 v[20:21], v[20:21], v[36:37], 0.5 op_sel_hi:[1,1,0] neg_lo:[1,0,0] neg_hi:[1,0,0]
	v_rcp_f32_e32 v45, v45
	v_pk_fma_f32 v[56:57], v[40:41], v[56:57], s[4:5] op_sel_hi:[1,1,0]
	v_pk_mul_f32 v[42:43], v[42:43], v[58:59]
	v_pk_fma_f32 v[24:25], v[24:25], v[38:39], 0.5 op_sel_hi:[1,1,0] neg_lo:[1,0,0] neg_hi:[1,0,0]
	v_pk_mul_f32 v[18:19], v[18:19], v[20:21]
	v_pk_mul_f32 v[40:41], v[40:41], v[56:57]
	v_pk_mul_f32 v[20:21], v[22:23], v[24:25]
	v_pk_fma_f32 v[0:1], v[0:1], 0.5, v[18:19] op_sel_hi:[1,0,1]
	v_pk_fma_f32 v[18:19], v[32:33], v[42:43], 0.5 op_sel_hi:[1,1,0] neg_lo:[1,0,0] neg_hi:[1,0,0]
	v_pk_fma_f32 v[28:29], v[28:29], v[40:41], 0.5 op_sel_hi:[1,1,0] neg_lo:[1,0,0] neg_hi:[1,0,0]
	v_pk_fma_f32 v[2:3], v[2:3], 0.5, v[20:21] op_sel_hi:[1,0,1]
	v_pk_mul_f32 v[18:19], v[30:31], v[18:19]
	v_pk_mul_f32 v[20:21], v[8:9], v[8:9]
	v_pk_mul_f32 v[22:23], v[26:27], v[28:29]
	v_pk_fma_f32 v[6:7], v[6:7], 0.5, v[18:19] op_sel_hi:[1,0,1]
	v_pk_fma_f32 v[18:19], v[44:45], s[8:9], v[16:17] op_sel_hi:[1,0,0]
	v_pk_mul_f32 v[20:21], v[20:21], s[6:7] op_sel_hi:[1,0]
	v_pk_mul_f32 v[10:11], v[218:219], v[54:55]
	v_pk_fma_f32 v[4:5], v[4:5], 0.5, v[22:23] op_sel_hi:[1,0,1]
	v_pk_fma_f32 v[18:19], v[44:45], v[18:19], s[10:11] op_sel_hi:[1,1,0]
	v_exp_f32_e32 v20, v20
	v_exp_f32_e32 v21, v21
	v_and_b32_e32 v23, 0x7fffffff, v11
	v_and_b32_e32 v22, 0x7fffffff, v10
	v_pk_fma_f32 v[18:19], v[44:45], v[18:19], s[2:3] op_sel_hi:[1,1,0]
	v_pk_fma_f32 v[24:25], v[22:23], s[12:13], 1.0 op_sel_hi:[1,0,0]
	v_pk_fma_f32 v[18:19], v[44:45], v[18:19], s[4:5] op_sel_hi:[1,1,0]
	v_rcp_f32_e32 v24, v24
	v_rcp_f32_e32 v25, v25
	v_pk_mul_f32 v[18:19], v[44:45], v[18:19]
	v_pk_mul_f32 v[12:13], v[220:221], v[48:49]
	v_pk_fma_f32 v[18:19], v[20:21], v[18:19], 0.5 op_sel_hi:[1,1,0] neg_lo:[1,0,0] neg_hi:[1,0,0]
	v_pk_mul_f32 v[20:21], v[10:11], v[10:11]
	v_pk_mul_f32 v[18:19], v[34:35], v[18:19]
	v_pk_mul_f32 v[20:21], v[20:21], s[6:7] op_sel_hi:[1,0]
	v_pk_fma_f32 v[8:9], v[8:9], 0.5, v[18:19] op_sel_hi:[1,0,1]
	v_pk_fma_f32 v[18:19], v[24:25], s[8:9], v[16:17] op_sel_hi:[1,0,0]
	v_exp_f32_e32 v20, v20
	v_pk_fma_f32 v[18:19], v[24:25], v[18:19], s[10:11] op_sel_hi:[1,1,0]
	v_exp_f32_e32 v21, v21
	v_pk_fma_f32 v[18:19], v[24:25], v[18:19], s[2:3] op_sel_hi:[1,1,0]
	v_pk_mul_f32 v[14:15], v[222:223], v[50:51]
	v_pk_fma_f32 v[18:19], v[24:25], v[18:19], s[4:5] op_sel_hi:[1,1,0]
	s_nop 0
	v_pk_mul_f32 v[18:19], v[24:25], v[18:19]
	v_and_b32_e32 v25, 0x7fffffff, v13
	v_and_b32_e32 v24, 0x7fffffff, v12
	v_pk_fma_f32 v[26:27], v[24:25], s[12:13], 1.0 op_sel_hi:[1,0,0]
	v_pk_fma_f32 v[18:19], v[20:21], v[18:19], 0.5 op_sel_hi:[1,1,0] neg_lo:[1,0,0] neg_hi:[1,0,0]
	v_rcp_f32_e32 v26, v26
	v_rcp_f32_e32 v27, v27
	v_pk_mul_f32 v[18:19], v[22:23], v[18:19]
	v_pk_mul_f32 v[20:21], v[12:13], v[12:13]
	v_pk_fma_f32 v[10:11], v[10:11], 0.5, v[18:19] op_sel_hi:[1,0,1]
	v_pk_fma_f32 v[18:19], v[26:27], s[8:9], v[16:17] op_sel_hi:[1,0,0]
	v_pk_mul_f32 v[20:21], v[20:21], s[6:7] op_sel_hi:[1,0]
	v_pk_fma_f32 v[18:19], v[26:27], v[18:19], s[10:11] op_sel_hi:[1,1,0]
	v_exp_f32_e32 v20, v20
	v_pk_fma_f32 v[18:19], v[26:27], v[18:19], s[2:3] op_sel_hi:[1,1,0]
	v_exp_f32_e32 v21, v21
	v_pk_fma_f32 v[18:19], v[26:27], v[18:19], s[4:5] op_sel_hi:[1,1,0]
	v_and_b32_e32 v23, 0x7fffffff, v15
	v_and_b32_e32 v22, 0x7fffffff, v14
	v_pk_mul_f32 v[18:19], v[26:27], v[18:19]
	v_pk_fma_f32 v[26:27], v[22:23], s[12:13], 1.0 op_sel_hi:[1,0,0]
	v_pk_fma_f32 v[18:19], v[20:21], v[18:19], 0.5 op_sel_hi:[1,1,0] neg_lo:[1,0,0] neg_hi:[1,0,0]
	v_rcp_f32_e32 v26, v26
	v_rcp_f32_e32 v27, v27
	v_pk_mul_f32 v[18:19], v[24:25], v[18:19]
	v_pk_fma_f32 v[16:17], v[26:27], s[8:9], v[16:17] op_sel_hi:[1,0,0]
	v_pk_fma_f32 v[12:13], v[12:13], 0.5, v[18:19] op_sel_hi:[1,0,1]
	v_pk_mul_f32 v[18:19], v[14:15], v[14:15]
	v_pk_fma_f32 v[16:17], v[26:27], v[16:17], s[10:11] op_sel_hi:[1,1,0]
	v_pk_mul_f32 v[18:19], v[18:19], s[6:7] op_sel_hi:[1,0]
	v_pk_fma_f32 v[16:17], v[26:27], v[16:17], s[2:3] op_sel_hi:[1,1,0]
	v_exp_f32_e32 v18, v18
	v_exp_f32_e32 v19, v19
	v_pk_fma_f32 v[16:17], v[26:27], v[16:17], s[4:5] op_sel_hi:[1,1,0]
	s_nop 0
	v_pk_mul_f32 v[16:17], v[26:27], v[16:17]
	s_nop 0
	v_pk_fma_f32 v[16:17], v[18:19], v[16:17], 0.5 op_sel_hi:[1,1,0] neg_lo:[1,0,0] neg_hi:[1,0,0]
	v_pk_mul_f32 v[16:17], v[22:23], v[16:17]
	s_nop 0
	v_pk_fma_f32 v[14:15], v[14:15], 0.5, v[16:17] op_sel_hi:[1,0,1]
	v_max3_f32 v16, |v6|, |v7|, |v0|
	v_max3_f32 v16, v16, |v1|, |v2|
	v_max3_f32 v16, v16, |v3|, |v4|
	v_max3_f32 v16, v16, |v5|, |v8|
	v_max3_f32 v16, v16, |v9|, |v10|
	v_max3_f32 v16, v16, |v11|, |v12|
	v_max3_f32 v16, v16, |v13|, |v14|
	v_max_f32_e64 v16, v16, |v15|
	v_mov_b32_e32 v17, v16
	s_nop 1
	v_permlane16_swap_b32_e32 v16, v17
	v_max_f32_e32 v16, v16, v17
	v_lshrrev_b32_e32 v17, 23, v16
	v_and_b32_e32 v16, 0x7fffff, v16
	v_cmp_lt_u32_e32 vcc, s3, v16
	s_nop 1
	v_addc_co_u32_e32 v16, vcc, v17, v64, vcc
	v_med3_i32 v48, v16, s5, v65
	v_lshlrev_b32_e32 v16, 23, v48
	v_sub_u32_e32 v16, 1.0, v16
	v_pk_mul_f32 v[40:41], v[16:17], v[8:9] op_sel_hi:[0,1]
	v_pk_mul_f32 v[42:43], v[16:17], v[10:11] op_sel_hi:[0,1]
	v_pk_mul_f32 v[44:45], v[16:17], v[12:13] op_sel_hi:[0,1]
	v_pk_mul_f32 v[46:47], v[16:17], v[14:15] op_sel_hi:[0,1]
	v_pk_mul_f32 v[32:33], v[16:17], v[0:1] op_sel_hi:[0,1]
	v_pk_mul_f32 v[34:35], v[16:17], v[2:3] op_sel_hi:[0,1]
	v_pk_mul_f32 v[36:37], v[16:17], v[4:5] op_sel_hi:[0,1]
	v_pk_mul_f32 v[38:39], v[16:17], v[6:7] op_sel_hi:[0,1]
	v_cvt_scalef32_2xpk16_fp6_f32 v[50:55], v[32:47], v[40:55], 1.0
	v_cvt_scalef32_pk32_f32_fp6 v[0:31], v[50:55], s7
	v_fma_f32 v16, v32, s14, v0
	v_fma_f32 v17, v33, s14, v2
	v_fma_f32 v18, v34, s14, v4
	v_fma_f32 v19, v35, s14, v6
	v_fma_f32 v20, v36, s14, v8
	v_fma_f32 v21, v37, s14, v10
	v_fma_f32 v22, v38, s14, v12
	v_fma_f32 v23, v39, s14, v14
	v_fma_f32 v24, v40, s14, v1
	v_fma_f32 v25, v41, s14, v3
	v_fma_f32 v26, v42, s14, v5
	v_fma_f32 v27, v43, s14, v7
	v_fma_f32 v28, v44, s14, v9
	v_fma_f32 v29, v45, s14, v11
	v_fma_f32 v30, v46, s14, v13
	v_fma_f32 v31, v47, s14, v15
	v_cvt_scalef32_2xpk16_fp6_f32 v[0:5], v[16:31], v[24:39], 1.0
	v_lshl_add_u64 v[4:5], v[118:119], 0, v[114:115]
	v_lshl_add_u64 v[4:5], v[4:5], 0, v[160:161]
	global_store_dwordx3 v[4:5], v[50:52], off nt
	v_add_co_u32_e32 v4, vcc, 0x1000, v4
	v_xor_b32_e32 v0, 0x20820820, v0
	v_xor_b32_e32 v1, 0x8208208, v1
	v_xor_b32_e32 v2, 0x82082082, v2
	v_addc_co_u32_e32 v5, vcc, 0, v5, vcc
	global_store_dwordx3 v[4:5], v[0:2], off offset:2048 nt
	s_and_saveexec_b64 s[2:3], s[0:1]
	s_cbranch_execz .LBB3_22
	v_mov_b32_e32 v1, 0x7a00
	v_add_u32_e32 v0, 0x7f, v48
	v_lshl_add_u32 v1, v48, 8, v1
	v_mov_b32_e32 v113, 0
	v_or_b32_e32 v2, v1, v0
	v_lshl_add_u64 v[0:1], v[116:117], 0, v[112:113]
	global_store_short v[0:1], v2, off
